# sc1 write-through on GEMM epilogue stores (cheaper barrier flush)
# speedup vs baseline: 1.5200x; 1.5200x over previous
.LBB0_219:
	s_xor_b64 s[24:25], s[24:25], -1
	v_mov_b32_e32 v149, v144
	v_mov_b32_e32 v148, v145
	s_cmp_gt_i32 s4, 24
	s_mov_b64 s[26:27], -1
	s_cbranch_scc0 .LBB0_221
	s_mul_i32 s21, s6, 24
	s_sub_i32 s23, s4, 25
	s_add_u32 s26, s21, s23
	s_mov_b32 s21, 0xc1f00000
	v_max_f32_e32 v143, v126, v126
	v_max_f32_e32 v153, v128, v128
	v_med3_f32 v143, v143, s21, v209
	v_med3_f32 v153, v153, s21, v209
	v_mul_f32_e32 v143, 0xbfb8aa3b, v143
	v_mul_f32_e32 v153, 0xbfb8aa3b, v153
	v_max_f32_e32 v142, v122, v122
	v_exp_f32_e32 v150, v143
	v_max_f32_e32 v143, v123, v123
	v_max_f32_e32 v151, v127, v127
	v_max_f32_e32 v152, v124, v124
	v_exp_f32_e32 v154, v153
	v_max_f32_e32 v153, v125, v125
	v_max_f32_e32 v155, v129, v129
	v_med3_f32 v142, v142, s21, v209
	v_med3_f32 v143, v143, s21, v209
	v_med3_f32 v151, v151, s21, v209
	v_med3_f32 v152, v152, s21, v209
	v_med3_f32 v153, v153, s21, v209
	v_med3_f32 v155, v155, s21, v209
	v_mul_f32_e32 v142, 0xbfb8aa3b, v142
	v_mul_f32_e32 v143, 0xbfb8aa3b, v143
	v_mul_f32_e32 v151, 0xbfb8aa3b, v151
	v_mul_f32_e32 v152, 0xbfb8aa3b, v152
	v_mul_f32_e32 v153, 0xbfb8aa3b, v153
	v_mul_f32_e32 v155, 0xbfb8aa3b, v155
	s_mul_hi_i32 s5, s6, 24
	v_exp_f32_e32 v142, v142
	v_exp_f32_e32 v143, v143
	v_exp_f32_e32 v151, v151
	v_exp_f32_e32 v152, v152
	v_exp_f32_e32 v153, v153
	v_exp_f32_e32 v155, v155
	s_addc_u32 s27, s5, 0
	s_lshl_b64 s[26:27], s[26:27], 17
	v_lshlrev_b32_e32 v140, 3, v149
	s_add_u32 s26, s48, s26
	v_lshl_add_u32 v140, v148, 7, v140
	s_addc_u32 s27, s49, s27
	v_ashrrev_i32_e32 v141, 31, v140
	v_pk_add_f32 v[142:143], v[142:143], 1.0 op_sel_hi:[1,0]
	v_pk_add_f32 v[156:157], v[150:151], 1.0 op_sel_hi:[1,0]
	v_pk_add_f32 v[152:153], v[152:153], 1.0 op_sel_hi:[1,0]
	v_pk_add_f32 v[154:155], v[154:155], 1.0 op_sel_hi:[1,0]
	v_lshl_add_u64 v[140:141], v[140:141], 1, s[26:27]
	v_cvt_pk_bf16_f32 v150, v142, v143
	v_cvt_pk_bf16_f32 v151, v152, v153
	v_cvt_pk_bf16_f32 v152, v156, v157
	v_cvt_pk_bf16_f32 v153, v154, v155
	global_store_dwordx4 v[140:141], v[150:153], off sc1
	v_max_f32_e32 v143, v114, v114
	v_med3_f32 v143, v143, s21, v209
	v_max_f32_e32 v153, v116, v116
	v_med3_f32 v153, v153, s21, v209
	v_mul_f32_e32 v143, 0xbfb8aa3b, v143
	v_mul_f32_e32 v153, 0xbfb8aa3b, v153
	v_max_f32_e32 v142, v118, v118
	v_exp_f32_e32 v150, v143
	v_max_f32_e32 v143, v119, v119
	v_max_f32_e32 v151, v115, v115
	v_max_f32_e32 v152, v120, v120
	v_exp_f32_e32 v154, v153
	v_max_f32_e32 v153, v121, v121
	v_max_f32_e32 v155, v117, v117
	v_med3_f32 v142, v142, s21, v209
	v_med3_f32 v143, v143, s21, v209
	v_med3_f32 v151, v151, s21, v209
	v_med3_f32 v152, v152, s21, v209
	v_med3_f32 v153, v153, s21, v209
	v_med3_f32 v155, v155, s21, v209
	v_mul_f32_e32 v142, 0xbfb8aa3b, v142
	v_mul_f32_e32 v143, 0xbfb8aa3b, v143
	v_mul_f32_e32 v151, 0xbfb8aa3b, v151
	v_mul_f32_e32 v152, 0xbfb8aa3b, v152
	v_mul_f32_e32 v153, 0xbfb8aa3b, v153
	v_mul_f32_e32 v155, 0xbfb8aa3b, v155
	v_exp_f32_e32 v142, v142
	v_exp_f32_e32 v143, v143
	v_exp_f32_e32 v151, v151
	v_exp_f32_e32 v152, v152
	v_exp_f32_e32 v153, v153
	v_exp_f32_e32 v155, v155
	v_pk_add_f32 v[142:143], v[142:143], 1.0 op_sel_hi:[1,0]
	v_pk_add_f32 v[156:157], v[150:151], 1.0 op_sel_hi:[1,0]
	v_pk_add_f32 v[152:153], v[152:153], 1.0 op_sel_hi:[1,0]
	v_pk_add_f32 v[154:155], v[154:155], 1.0 op_sel_hi:[1,0]
	v_cvt_pk_bf16_f32 v150, v142, v143
	v_cvt_pk_bf16_f32 v151, v152, v153
	v_cvt_pk_bf16_f32 v152, v156, v157
	v_cvt_pk_bf16_f32 v153, v154, v155
	global_store_dwordx4 v[140:141], v[150:153], off offset:1024 sc1
	v_max_f32_e32 v143, v106, v106
	v_med3_f32 v143, v143, s21, v209
	v_max_f32_e32 v153, v108, v108
	v_med3_f32 v153, v153, s21, v209
	v_mul_f32_e32 v143, 0xbfb8aa3b, v143
	v_mul_f32_e32 v153, 0xbfb8aa3b, v153
	v_max_f32_e32 v142, v110, v110
	v_exp_f32_e32 v150, v143
	v_max_f32_e32 v143, v111, v111
	v_max_f32_e32 v151, v107, v107
	v_max_f32_e32 v152, v112, v112
	v_exp_f32_e32 v154, v153
	v_max_f32_e32 v153, v113, v113
	v_max_f32_e32 v155, v109, v109
	v_med3_f32 v142, v142, s21, v209
	v_med3_f32 v143, v143, s21, v209
	v_med3_f32 v151, v151, s21, v209
	v_med3_f32 v152, v152, s21, v209
	v_med3_f32 v153, v153, s21, v209
	v_med3_f32 v155, v155, s21, v209
	v_mul_f32_e32 v142, 0xbfb8aa3b, v142
	v_mul_f32_e32 v143, 0xbfb8aa3b, v143
	v_mul_f32_e32 v151, 0xbfb8aa3b, v151
	v_mul_f32_e32 v152, 0xbfb8aa3b, v152
	v_mul_f32_e32 v153, 0xbfb8aa3b, v153
	v_mul_f32_e32 v155, 0xbfb8aa3b, v155
	v_exp_f32_e32 v142, v142
	v_exp_f32_e32 v143, v143
	v_exp_f32_e32 v151, v151
	v_exp_f32_e32 v152, v152
	v_exp_f32_e32 v153, v153
	v_exp_f32_e32 v155, v155
	v_pk_add_f32 v[142:143], v[142:143], 1.0 op_sel_hi:[1,0]
	v_pk_add_f32 v[156:157], v[150:151], 1.0 op_sel_hi:[1,0]
	v_pk_add_f32 v[152:153], v[152:153], 1.0 op_sel_hi:[1,0]
	v_pk_add_f32 v[154:155], v[154:155], 1.0 op_sel_hi:[1,0]
	v_cvt_pk_bf16_f32 v150, v142, v143
	v_cvt_pk_bf16_f32 v151, v152, v153
	v_cvt_pk_bf16_f32 v152, v156, v157
	v_cvt_pk_bf16_f32 v153, v154, v155
	global_store_dwordx4 v[140:141], v[150:153], off offset:2048 sc1
	v_max_f32_e32 v143, v98, v98
	v_med3_f32 v143, v143, s21, v209
	v_max_f32_e32 v153, v100, v100
	v_med3_f32 v153, v153, s21, v209
	v_mul_f32_e32 v143, 0xbfb8aa3b, v143
	v_mul_f32_e32 v153, 0xbfb8aa3b, v153
	v_max_f32_e32 v142, v102, v102
	v_exp_f32_e32 v150, v143
	v_max_f32_e32 v143, v103, v103
	v_max_f32_e32 v151, v99, v99
	v_max_f32_e32 v152, v104, v104
	v_exp_f32_e32 v154, v153
	v_max_f32_e32 v153, v105, v105
	v_max_f32_e32 v155, v101, v101
	v_med3_f32 v142, v142, s21, v209
	v_med3_f32 v143, v143, s21, v209
	v_med3_f32 v151, v151, s21, v209
	v_med3_f32 v152, v152, s21, v209
	v_med3_f32 v153, v153, s21, v209
	v_med3_f32 v155, v155, s21, v209
	v_mul_f32_e32 v142, 0xbfb8aa3b, v142
	v_mul_f32_e32 v143, 0xbfb8aa3b, v143
	v_mul_f32_e32 v151, 0xbfb8aa3b, v151
	v_mul_f32_e32 v152, 0xbfb8aa3b, v152
	v_mul_f32_e32 v153, 0xbfb8aa3b, v153
	v_mul_f32_e32 v155, 0xbfb8aa3b, v155
	v_exp_f32_e32 v142, v142
	v_exp_f32_e32 v143, v143
	v_exp_f32_e32 v151, v151
	v_exp_f32_e32 v152, v152
	v_exp_f32_e32 v153, v153
	v_exp_f32_e32 v155, v155
	v_pk_add_f32 v[142:143], v[142:143], 1.0 op_sel_hi:[1,0]
	v_pk_add_f32 v[156:157], v[150:151], 1.0 op_sel_hi:[1,0]
	v_pk_add_f32 v[152:153], v[152:153], 1.0 op_sel_hi:[1,0]
	v_pk_add_f32 v[154:155], v[154:155], 1.0 op_sel_hi:[1,0]
	v_cvt_pk_bf16_f32 v150, v142, v143
	v_cvt_pk_bf16_f32 v151, v152, v153
	v_cvt_pk_bf16_f32 v152, v156, v157
	v_cvt_pk_bf16_f32 v153, v154, v155
	global_store_dwordx4 v[140:141], v[150:153], off offset:3072 sc1
	v_max_f32_e32 v143, v88, v88
	v_med3_f32 v143, v143, s21, v209
	v_max_f32_e32 v153, v90, v90
	v_med3_f32 v153, v153, s21, v209
	v_mul_f32_e32 v153, 0xbfb8aa3b, v153
	v_max_f32_e32 v152, v94, v94
	v_exp_f32_e32 v154, v153
	v_max_f32_e32 v153, v95, v95
	v_max_f32_e32 v155, v91, v91
	v_mul_f32_e32 v143, 0xbfb8aa3b, v143
	v_max_f32_e32 v151, v89, v89
	v_med3_f32 v152, v152, s21, v209
	v_med3_f32 v153, v153, s21, v209
	v_med3_f32 v155, v155, s21, v209
	v_max_f32_e32 v142, v92, v92
	v_exp_f32_e32 v150, v143
	v_max_f32_e32 v143, v93, v93
	v_med3_f32 v151, v151, s21, v209
	v_mul_f32_e32 v152, 0xbfb8aa3b, v152
	v_mul_f32_e32 v153, 0xbfb8aa3b, v153
	v_mul_f32_e32 v155, 0xbfb8aa3b, v155
	v_med3_f32 v142, v142, s21, v209
	v_med3_f32 v143, v143, s21, v209
	v_mul_f32_e32 v151, 0xbfb8aa3b, v151
	v_exp_f32_e32 v152, v152
	v_exp_f32_e32 v153, v153
	v_exp_f32_e32 v155, v155
	v_mul_f32_e32 v142, 0xbfb8aa3b, v142
	v_mul_f32_e32 v143, 0xbfb8aa3b, v143
	v_exp_f32_e32 v151, v151
	v_exp_f32_e32 v142, v142
	v_exp_f32_e32 v143, v143
	v_pk_add_f32 v[152:153], v[152:153], 1.0 op_sel_hi:[1,0]
	v_pk_add_f32 v[154:155], v[154:155], 1.0 op_sel_hi:[1,0]
	s_movk_i32 s5, 0x1000
	v_pk_add_f32 v[156:157], v[150:151], 1.0 op_sel_hi:[1,0]
	v_cvt_pk_bf16_f32 v151, v152, v153
	v_cvt_pk_bf16_f32 v153, v154, v155
	v_add_co_u32_e32 v154, vcc, s5, v140
	v_pk_add_f32 v[142:143], v[142:143], 1.0 op_sel_hi:[1,0]
	s_nop 0
	v_addc_co_u32_e32 v155, vcc, 0, v141, vcc
	s_movk_i32 s5, 0x2000
	v_cvt_pk_bf16_f32 v150, v142, v143
	v_add_co_u32_e32 v142, vcc, s5, v140
	v_cvt_pk_bf16_f32 v152, v156, v157
	s_nop 0
	v_addc_co_u32_e32 v143, vcc, 0, v141, vcc
	global_store_dwordx4 v[142:143], v[150:153], off offset:-4096 sc1
	v_max_f32_e32 v157, v82, v82
	v_med3_f32 v157, v157, s21, v209
	v_max_f32_e32 v151, v80, v80
	v_med3_f32 v151, v151, s21, v209
	v_mul_f32_e32 v151, 0xbfb8aa3b, v151
	v_mul_f32_e32 v157, 0xbfb8aa3b, v157
	v_max_f32_e32 v150, v84, v84
	v_exp_f32_e32 v152, v151
	v_max_f32_e32 v151, v85, v85
	v_max_f32_e32 v153, v81, v81
	v_max_f32_e32 v156, v86, v86
	v_exp_f32_e32 v158, v157
	v_max_f32_e32 v157, v87, v87
	v_max_f32_e32 v159, v83, v83
	v_med3_f32 v150, v150, s21, v209
	v_med3_f32 v151, v151, s21, v209
	v_med3_f32 v153, v153, s21, v209
	v_med3_f32 v156, v156, s21, v209
	v_med3_f32 v157, v157, s21, v209
	v_med3_f32 v159, v159, s21, v209
	v_mul_f32_e32 v150, 0xbfb8aa3b, v150
	v_mul_f32_e32 v151, 0xbfb8aa3b, v151
	v_mul_f32_e32 v153, 0xbfb8aa3b, v153
	v_mul_f32_e32 v156, 0xbfb8aa3b, v156
	v_mul_f32_e32 v157, 0xbfb8aa3b, v157
	v_mul_f32_e32 v159, 0xbfb8aa3b, v159
	v_exp_f32_e32 v150, v150
	v_exp_f32_e32 v151, v151
	v_exp_f32_e32 v153, v153
	v_exp_f32_e32 v156, v156
	v_exp_f32_e32 v157, v157
	v_exp_f32_e32 v159, v159
	v_pk_add_f32 v[150:151], v[150:151], 1.0 op_sel_hi:[1,0]
	v_pk_add_f32 v[152:153], v[152:153], 1.0 op_sel_hi:[1,0]
	v_pk_add_f32 v[156:157], v[156:157], 1.0 op_sel_hi:[1,0]
	v_pk_add_f32 v[158:159], v[158:159], 1.0 op_sel_hi:[1,0]
	v_cvt_pk_bf16_f32 v150, v150, v151
	v_cvt_pk_bf16_f32 v151, v156, v157
	v_cvt_pk_bf16_f32 v152, v152, v153
	v_cvt_pk_bf16_f32 v153, v158, v159
	global_store_dwordx4 v[154:155], v[150:153], off offset:1024 sc1
	v_max_f32_e32 v157, v74, v74
	v_med3_f32 v157, v157, s21, v209
	v_max_f32_e32 v151, v72, v72
	v_med3_f32 v151, v151, s21, v209
	v_mul_f32_e32 v151, 0xbfb8aa3b, v151
	v_mul_f32_e32 v157, 0xbfb8aa3b, v157
	v_max_f32_e32 v150, v76, v76
	v_exp_f32_e32 v152, v151
	v_max_f32_e32 v151, v77, v77
	v_max_f32_e32 v153, v73, v73
	v_max_f32_e32 v156, v78, v78
	v_exp_f32_e32 v158, v157
	v_max_f32_e32 v157, v79, v79
	v_max_f32_e32 v159, v75, v75
	v_med3_f32 v150, v150, s21, v209
	v_med3_f32 v151, v151, s21, v209
	v_med3_f32 v153, v153, s21, v209
	v_med3_f32 v156, v156, s21, v209
	v_med3_f32 v157, v157, s21, v209
	v_med3_f32 v159, v159, s21, v209
	v_mul_f32_e32 v150, 0xbfb8aa3b, v150
	v_mul_f32_e32 v151, 0xbfb8aa3b, v151
	v_mul_f32_e32 v153, 0xbfb8aa3b, v153
	v_mul_f32_e32 v156, 0xbfb8aa3b, v156
	v_mul_f32_e32 v157, 0xbfb8aa3b, v157
	v_mul_f32_e32 v159, 0xbfb8aa3b, v159
	v_exp_f32_e32 v150, v150
	v_exp_f32_e32 v151, v151
	v_exp_f32_e32 v153, v153
	v_exp_f32_e32 v156, v156
	v_exp_f32_e32 v157, v157
	v_exp_f32_e32 v159, v159
	v_pk_add_f32 v[150:151], v[150:151], 1.0 op_sel_hi:[1,0]
	v_pk_add_f32 v[152:153], v[152:153], 1.0 op_sel_hi:[1,0]
	v_pk_add_f32 v[156:157], v[156:157], 1.0 op_sel_hi:[1,0]
	v_pk_add_f32 v[158:159], v[158:159], 1.0 op_sel_hi:[1,0]
	v_cvt_pk_bf16_f32 v150, v150, v151
	v_cvt_pk_bf16_f32 v151, v156, v157
	v_cvt_pk_bf16_f32 v152, v152, v153
	v_cvt_pk_bf16_f32 v153, v158, v159
	global_store_dwordx4 v[154:155], v[150:153], off offset:2048 sc1
	v_max_f32_e32 v157, v66, v66
	v_med3_f32 v157, v157, s21, v209
	v_max_f32_e32 v151, v64, v64
	v_med3_f32 v151, v151, s21, v209
	v_mul_f32_e32 v151, 0xbfb8aa3b, v151
	v_mul_f32_e32 v157, 0xbfb8aa3b, v157
	v_max_f32_e32 v150, v68, v68
	v_exp_f32_e32 v152, v151
	v_max_f32_e32 v151, v69, v69
	v_max_f32_e32 v153, v65, v65
	v_max_f32_e32 v156, v70, v70
	v_exp_f32_e32 v158, v157
	v_max_f32_e32 v157, v71, v71
	v_max_f32_e32 v159, v67, v67
	v_med3_f32 v150, v150, s21, v209
	v_med3_f32 v151, v151, s21, v209
	v_med3_f32 v153, v153, s21, v209
	v_med3_f32 v156, v156, s21, v209
	v_med3_f32 v157, v157, s21, v209
	v_med3_f32 v159, v159, s21, v209
	v_mul_f32_e32 v150, 0xbfb8aa3b, v150
	v_mul_f32_e32 v151, 0xbfb8aa3b, v151
	v_mul_f32_e32 v153, 0xbfb8aa3b, v153
	v_mul_f32_e32 v156, 0xbfb8aa3b, v156
	v_mul_f32_e32 v157, 0xbfb8aa3b, v157
	v_mul_f32_e32 v159, 0xbfb8aa3b, v159
	v_exp_f32_e32 v150, v150
	v_exp_f32_e32 v151, v151
	v_exp_f32_e32 v153, v153
	v_exp_f32_e32 v156, v156
	v_exp_f32_e32 v157, v157
	v_exp_f32_e32 v159, v159
	v_pk_add_f32 v[150:151], v[150:151], 1.0 op_sel_hi:[1,0]
	v_pk_add_f32 v[152:153], v[152:153], 1.0 op_sel_hi:[1,0]
	v_pk_add_f32 v[156:157], v[156:157], 1.0 op_sel_hi:[1,0]
	v_pk_add_f32 v[158:159], v[158:159], 1.0 op_sel_hi:[1,0]
	v_cvt_pk_bf16_f32 v150, v150, v151
	v_cvt_pk_bf16_f32 v151, v156, v157
	v_cvt_pk_bf16_f32 v152, v152, v153
	v_cvt_pk_bf16_f32 v153, v158, v159
	global_store_dwordx4 v[154:155], v[150:153], off offset:3072 sc1
	v_max_f32_e32 v155, v58, v58
	v_med3_f32 v155, v155, s21, v209
	v_max_f32_e32 v151, v56, v56
	v_med3_f32 v151, v151, s21, v209
	v_mul_f32_e32 v151, 0xbfb8aa3b, v151
	v_mul_f32_e32 v155, 0xbfb8aa3b, v155
	v_max_f32_e32 v150, v60, v60
	v_exp_f32_e32 v152, v151
	v_max_f32_e32 v151, v61, v61
	v_max_f32_e32 v153, v57, v57
	v_max_f32_e32 v154, v62, v62
	v_exp_f32_e32 v156, v155
	v_max_f32_e32 v155, v63, v63
	v_max_f32_e32 v157, v59, v59
	v_med3_f32 v150, v150, s21, v209
	v_med3_f32 v151, v151, s21, v209
	v_med3_f32 v153, v153, s21, v209
	v_med3_f32 v154, v154, s21, v209
	v_med3_f32 v155, v155, s21, v209
	v_med3_f32 v157, v157, s21, v209
	v_mul_f32_e32 v150, 0xbfb8aa3b, v150
	v_mul_f32_e32 v151, 0xbfb8aa3b, v151
	v_mul_f32_e32 v153, 0xbfb8aa3b, v153
	v_mul_f32_e32 v154, 0xbfb8aa3b, v154
	v_mul_f32_e32 v155, 0xbfb8aa3b, v155
	v_mul_f32_e32 v157, 0xbfb8aa3b, v157
	v_exp_f32_e32 v150, v150
	v_exp_f32_e32 v151, v151
	v_exp_f32_e32 v153, v153
	v_exp_f32_e32 v154, v154
	v_exp_f32_e32 v155, v155
	v_exp_f32_e32 v157, v157
	v_pk_add_f32 v[150:151], v[150:151], 1.0 op_sel_hi:[1,0]
	v_pk_add_f32 v[152:153], v[152:153], 1.0 op_sel_hi:[1,0]
	v_pk_add_f32 v[154:155], v[154:155], 1.0 op_sel_hi:[1,0]
	v_pk_add_f32 v[156:157], v[156:157], 1.0 op_sel_hi:[1,0]
	v_cvt_pk_bf16_f32 v150, v150, v151
	v_cvt_pk_bf16_f32 v151, v154, v155
	v_cvt_pk_bf16_f32 v152, v152, v153
	v_cvt_pk_bf16_f32 v153, v156, v157
	global_store_dwordx4 v[142:143], v[150:153], off sc1
	v_max_f32_e32 v155, v50, v50
	v_med3_f32 v155, v155, s21, v209
	v_max_f32_e32 v151, v48, v48
	v_med3_f32 v151, v151, s21, v209
	v_mul_f32_e32 v151, 0xbfb8aa3b, v151
	v_mul_f32_e32 v155, 0xbfb8aa3b, v155
	v_max_f32_e32 v150, v52, v52
	v_exp_f32_e32 v152, v151
	v_max_f32_e32 v151, v53, v53
	v_max_f32_e32 v153, v49, v49
	v_max_f32_e32 v154, v54, v54
	v_exp_f32_e32 v156, v155
	v_max_f32_e32 v155, v55, v55
	v_max_f32_e32 v157, v51, v51
	v_med3_f32 v150, v150, s21, v209
	v_med3_f32 v151, v151, s21, v209
	v_med3_f32 v153, v153, s21, v209
	v_med3_f32 v154, v154, s21, v209
	v_med3_f32 v155, v155, s21, v209
	v_med3_f32 v157, v157, s21, v209
	v_mul_f32_e32 v150, 0xbfb8aa3b, v150
	v_mul_f32_e32 v151, 0xbfb8aa3b, v151
	v_mul_f32_e32 v153, 0xbfb8aa3b, v153
	v_mul_f32_e32 v154, 0xbfb8aa3b, v154
	v_mul_f32_e32 v155, 0xbfb8aa3b, v155
	v_mul_f32_e32 v157, 0xbfb8aa3b, v157
	v_exp_f32_e32 v150, v150
	v_exp_f32_e32 v151, v151
	v_exp_f32_e32 v153, v153
	v_exp_f32_e32 v154, v154
	v_exp_f32_e32 v155, v155
	v_exp_f32_e32 v157, v157
	v_pk_add_f32 v[150:151], v[150:151], 1.0 op_sel_hi:[1,0]
	v_pk_add_f32 v[152:153], v[152:153], 1.0 op_sel_hi:[1,0]
	v_pk_add_f32 v[154:155], v[154:155], 1.0 op_sel_hi:[1,0]
	v_pk_add_f32 v[156:157], v[156:157], 1.0 op_sel_hi:[1,0]
	v_cvt_pk_bf16_f32 v150, v150, v151
	v_cvt_pk_bf16_f32 v151, v154, v155
	v_cvt_pk_bf16_f32 v152, v152, v153
	v_cvt_pk_bf16_f32 v153, v156, v157
	global_store_dwordx4 v[142:143], v[150:153], off offset:1024 sc1
	v_max_f32_e32 v155, v42, v42
	v_med3_f32 v155, v155, s21, v209
	v_max_f32_e32 v151, v40, v40
	v_med3_f32 v151, v151, s21, v209
	v_mul_f32_e32 v151, 0xbfb8aa3b, v151
	v_mul_f32_e32 v155, 0xbfb8aa3b, v155
	v_max_f32_e32 v150, v44, v44
	v_exp_f32_e32 v152, v151
	v_max_f32_e32 v151, v45, v45
	v_max_f32_e32 v153, v41, v41
	v_max_f32_e32 v154, v46, v46
	v_exp_f32_e32 v156, v155
	v_max_f32_e32 v155, v47, v47
	v_max_f32_e32 v157, v43, v43
	v_med3_f32 v150, v150, s21, v209
	v_med3_f32 v151, v151, s21, v209
	v_med3_f32 v153, v153, s21, v209
	v_med3_f32 v154, v154, s21, v209
	v_med3_f32 v155, v155, s21, v209
	v_med3_f32 v157, v157, s21, v209
	v_mul_f32_e32 v150, 0xbfb8aa3b, v150
	v_mul_f32_e32 v151, 0xbfb8aa3b, v151
	v_mul_f32_e32 v153, 0xbfb8aa3b, v153
	v_mul_f32_e32 v154, 0xbfb8aa3b, v154
	v_mul_f32_e32 v155, 0xbfb8aa3b, v155
	v_mul_f32_e32 v157, 0xbfb8aa3b, v157
	v_exp_f32_e32 v150, v150
	v_exp_f32_e32 v151, v151
	v_exp_f32_e32 v153, v153
	v_exp_f32_e32 v154, v154
	v_exp_f32_e32 v155, v155
	v_exp_f32_e32 v157, v157
	v_pk_add_f32 v[150:151], v[150:151], 1.0 op_sel_hi:[1,0]
	v_pk_add_f32 v[152:153], v[152:153], 1.0 op_sel_hi:[1,0]
	v_pk_add_f32 v[154:155], v[154:155], 1.0 op_sel_hi:[1,0]
	v_pk_add_f32 v[156:157], v[156:157], 1.0 op_sel_hi:[1,0]
	v_cvt_pk_bf16_f32 v150, v150, v151
	v_cvt_pk_bf16_f32 v151, v154, v155
	v_cvt_pk_bf16_f32 v152, v152, v153
	v_cvt_pk_bf16_f32 v153, v156, v157
	global_store_dwordx4 v[142:143], v[150:153], off offset:2048 sc1
	v_max_f32_e32 v155, v34, v34
	v_med3_f32 v155, v155, s21, v209
	v_max_f32_e32 v151, v32, v32
	v_med3_f32 v151, v151, s21, v209
	v_mul_f32_e32 v151, 0xbfb8aa3b, v151
	v_mul_f32_e32 v155, 0xbfb8aa3b, v155
	v_max_f32_e32 v150, v36, v36
	v_exp_f32_e32 v152, v151
	v_max_f32_e32 v151, v37, v37
	v_max_f32_e32 v153, v33, v33
	v_max_f32_e32 v154, v38, v38
	v_exp_f32_e32 v156, v155
	v_max_f32_e32 v155, v39, v39
	v_max_f32_e32 v157, v35, v35
	v_med3_f32 v150, v150, s21, v209
	v_med3_f32 v151, v151, s21, v209
	v_med3_f32 v153, v153, s21, v209
	v_med3_f32 v154, v154, s21, v209
	v_med3_f32 v155, v155, s21, v209
	v_med3_f32 v157, v157, s21, v209
	v_mul_f32_e32 v150, 0xbfb8aa3b, v150
	v_mul_f32_e32 v151, 0xbfb8aa3b, v151
	v_mul_f32_e32 v153, 0xbfb8aa3b, v153
	v_mul_f32_e32 v154, 0xbfb8aa3b, v154
	v_mul_f32_e32 v155, 0xbfb8aa3b, v155
	v_mul_f32_e32 v157, 0xbfb8aa3b, v157
	v_exp_f32_e32 v150, v150
	v_exp_f32_e32 v151, v151
	v_exp_f32_e32 v153, v153
	v_exp_f32_e32 v154, v154
	v_exp_f32_e32 v155, v155
	v_exp_f32_e32 v157, v157
	v_pk_add_f32 v[150:151], v[150:151], 1.0 op_sel_hi:[1,0]
	v_pk_add_f32 v[152:153], v[152:153], 1.0 op_sel_hi:[1,0]
	v_pk_add_f32 v[154:155], v[154:155], 1.0 op_sel_hi:[1,0]
	v_pk_add_f32 v[156:157], v[156:157], 1.0 op_sel_hi:[1,0]
	v_cvt_pk_bf16_f32 v150, v150, v151
	v_cvt_pk_bf16_f32 v151, v154, v155
	v_cvt_pk_bf16_f32 v152, v152, v153
	v_cvt_pk_bf16_f32 v153, v156, v157
	global_store_dwordx4 v[142:143], v[150:153], off offset:3072 sc1
	v_max_f32_e32 v143, v24, v24
	v_med3_f32 v143, v143, s21, v209
	v_max_f32_e32 v153, v26, v26
	v_med3_f32 v153, v153, s21, v209
	v_mul_f32_e32 v153, 0xbfb8aa3b, v153
	v_mul_f32_e32 v143, 0xbfb8aa3b, v143
	v_max_f32_e32 v152, v30, v30
	v_exp_f32_e32 v154, v153
	v_max_f32_e32 v153, v31, v31
	v_max_f32_e32 v155, v27, v27
	v_max_f32_e32 v142, v28, v28
	v_exp_f32_e32 v150, v143
	v_max_f32_e32 v143, v29, v29
	v_max_f32_e32 v151, v25, v25
	v_med3_f32 v152, v152, s21, v209
	v_med3_f32 v153, v153, s21, v209
	v_med3_f32 v155, v155, s21, v209
	v_med3_f32 v142, v142, s21, v209
	v_med3_f32 v143, v143, s21, v209
	v_med3_f32 v151, v151, s21, v209
	v_mul_f32_e32 v152, 0xbfb8aa3b, v152
	v_mul_f32_e32 v153, 0xbfb8aa3b, v153
	v_mul_f32_e32 v155, 0xbfb8aa3b, v155
	v_mul_f32_e32 v142, 0xbfb8aa3b, v142
	v_mul_f32_e32 v143, 0xbfb8aa3b, v143
	v_mul_f32_e32 v151, 0xbfb8aa3b, v151
	v_exp_f32_e32 v152, v152
	v_exp_f32_e32 v153, v153
	v_exp_f32_e32 v155, v155
	v_exp_f32_e32 v142, v142
	v_exp_f32_e32 v143, v143
	v_exp_f32_e32 v151, v151
	v_pk_add_f32 v[152:153], v[152:153], 1.0 op_sel_hi:[1,0]
	v_pk_add_f32 v[154:155], v[154:155], 1.0 op_sel_hi:[1,0]
	s_movk_i32 s5, 0x3000
	v_pk_add_f32 v[142:143], v[142:143], 1.0 op_sel_hi:[1,0]
	v_pk_add_f32 v[156:157], v[150:151], 1.0 op_sel_hi:[1,0]
	v_cvt_pk_bf16_f32 v151, v152, v153
	v_cvt_pk_bf16_f32 v153, v154, v155
	v_add_co_u32_e32 v154, vcc, s5, v140
	v_cvt_pk_bf16_f32 v150, v142, v143
	v_cvt_pk_bf16_f32 v152, v156, v157
	v_addc_co_u32_e32 v155, vcc, 0, v141, vcc
	global_store_dwordx4 v[154:155], v[150:153], off sc1
	v_max_f32_e32 v141, v16, v16
	v_med3_f32 v141, v141, s21, v209
	v_max_f32_e32 v151, v18, v18
	v_med3_f32 v151, v151, s21, v209
	v_mul_f32_e32 v141, 0xbfb8aa3b, v141
	v_mul_f32_e32 v151, 0xbfb8aa3b, v151
	v_max_f32_e32 v140, v20, v20
	v_exp_f32_e32 v142, v141
	v_max_f32_e32 v141, v21, v21
	v_max_f32_e32 v143, v17, v17
	v_max_f32_e32 v150, v22, v22
	v_exp_f32_e32 v152, v151
	v_max_f32_e32 v151, v23, v23
	v_max_f32_e32 v153, v19, v19
	v_med3_f32 v140, v140, s21, v209
	v_med3_f32 v141, v141, s21, v209
	v_med3_f32 v143, v143, s21, v209
	v_med3_f32 v150, v150, s21, v209
	v_med3_f32 v151, v151, s21, v209
	v_med3_f32 v153, v153, s21, v209
	v_mul_f32_e32 v140, 0xbfb8aa3b, v140
	v_mul_f32_e32 v141, 0xbfb8aa3b, v141
	v_mul_f32_e32 v143, 0xbfb8aa3b, v143
	v_mul_f32_e32 v150, 0xbfb8aa3b, v150
	v_mul_f32_e32 v151, 0xbfb8aa3b, v151
	v_mul_f32_e32 v153, 0xbfb8aa3b, v153
	v_exp_f32_e32 v140, v140
	v_exp_f32_e32 v141, v141
	v_exp_f32_e32 v143, v143
	v_exp_f32_e32 v150, v150
	v_exp_f32_e32 v151, v151
	v_exp_f32_e32 v153, v153
	v_pk_add_f32 v[140:141], v[140:141], 1.0 op_sel_hi:[1,0]
	v_pk_add_f32 v[142:143], v[142:143], 1.0 op_sel_hi:[1,0]
	v_pk_add_f32 v[150:151], v[150:151], 1.0 op_sel_hi:[1,0]
	v_pk_add_f32 v[152:153], v[152:153], 1.0 op_sel_hi:[1,0]
	v_cvt_pk_bf16_f32 v140, v140, v141
	v_cvt_pk_bf16_f32 v141, v150, v151
	v_cvt_pk_bf16_f32 v142, v142, v143
	v_cvt_pk_bf16_f32 v143, v152, v153
	global_store_dwordx4 v[154:155], v[140:143], off offset:1024 sc1
	v_max_f32_e32 v151, v10, v10
	v_med3_f32 v151, v151, s21, v209
	v_max_f32_e32 v141, v8, v8
	v_med3_f32 v141, v141, s21, v209
	v_mul_f32_e32 v141, 0xbfb8aa3b, v141
	v_mul_f32_e32 v151, 0xbfb8aa3b, v151
	v_max_f32_e32 v140, v12, v12
	v_exp_f32_e32 v142, v141
	v_max_f32_e32 v141, v13, v13
	v_max_f32_e32 v143, v9, v9
	v_max_f32_e32 v150, v14, v14
	v_exp_f32_e32 v152, v151
	v_max_f32_e32 v151, v15, v15
	v_max_f32_e32 v153, v11, v11
	v_med3_f32 v140, v140, s21, v209
	v_med3_f32 v141, v141, s21, v209
	v_med3_f32 v143, v143, s21, v209
	v_med3_f32 v150, v150, s21, v209
	v_med3_f32 v151, v151, s21, v209
	v_med3_f32 v153, v153, s21, v209
	v_mul_f32_e32 v140, 0xbfb8aa3b, v140
	v_mul_f32_e32 v141, 0xbfb8aa3b, v141
	v_mul_f32_e32 v143, 0xbfb8aa3b, v143
	v_mul_f32_e32 v150, 0xbfb8aa3b, v150
	v_mul_f32_e32 v151, 0xbfb8aa3b, v151
	v_mul_f32_e32 v153, 0xbfb8aa3b, v153
	v_exp_f32_e32 v140, v140
	v_exp_f32_e32 v141, v141
	v_exp_f32_e32 v143, v143
	v_exp_f32_e32 v150, v150
	v_exp_f32_e32 v151, v151
	v_exp_f32_e32 v153, v153
	v_pk_add_f32 v[140:141], v[140:141], 1.0 op_sel_hi:[1,0]
	v_pk_add_f32 v[142:143], v[142:143], 1.0 op_sel_hi:[1,0]
	v_pk_add_f32 v[150:151], v[150:151], 1.0 op_sel_hi:[1,0]
	v_pk_add_f32 v[152:153], v[152:153], 1.0 op_sel_hi:[1,0]
	v_cvt_pk_bf16_f32 v140, v140, v141
	v_cvt_pk_bf16_f32 v141, v150, v151
	v_cvt_pk_bf16_f32 v142, v142, v143
	v_cvt_pk_bf16_f32 v143, v152, v153
	global_store_dwordx4 v[154:155], v[140:143], off offset:2048 sc1
	v_max_f32_e32 v151, v2, v2
	v_med3_f32 v151, v151, s21, v209
	v_max_f32_e32 v141, v0, v0
	v_med3_f32 v141, v141, s21, v209
	v_mul_f32_e32 v141, 0xbfb8aa3b, v141
	v_mul_f32_e32 v151, 0xbfb8aa3b, v151
	v_max_f32_e32 v140, v4, v4
	v_exp_f32_e32 v142, v141
	v_max_f32_e32 v141, v5, v5
	v_max_f32_e32 v143, v1, v1
	v_max_f32_e32 v150, v6, v6
	v_exp_f32_e32 v152, v151
	v_max_f32_e32 v151, v7, v7
	v_max_f32_e32 v153, v3, v3
	v_med3_f32 v140, v140, s21, v209
	v_med3_f32 v141, v141, s21, v209
	v_med3_f32 v143, v143, s21, v209
	v_med3_f32 v150, v150, s21, v209
	v_med3_f32 v151, v151, s21, v209
	v_med3_f32 v153, v153, s21, v209
	v_mul_f32_e32 v140, 0xbfb8aa3b, v140
	v_mul_f32_e32 v141, 0xbfb8aa3b, v141
	v_mul_f32_e32 v143, 0xbfb8aa3b, v143
	v_mul_f32_e32 v150, 0xbfb8aa3b, v150
	v_mul_f32_e32 v151, 0xbfb8aa3b, v151
	v_mul_f32_e32 v153, 0xbfb8aa3b, v153
	v_exp_f32_e32 v140, v140
	v_exp_f32_e32 v141, v141
	v_exp_f32_e32 v143, v143
	v_exp_f32_e32 v150, v150
	v_exp_f32_e32 v151, v151
	v_exp_f32_e32 v153, v153
	v_pk_add_f32 v[140:141], v[140:141], 1.0 op_sel_hi:[1,0]
	v_pk_add_f32 v[142:143], v[142:143], 1.0 op_sel_hi:[1,0]
	v_pk_add_f32 v[150:151], v[150:151], 1.0 op_sel_hi:[1,0]
	v_pk_add_f32 v[152:153], v[152:153], 1.0 op_sel_hi:[1,0]
	v_cvt_pk_bf16_f32 v140, v140, v141
	v_cvt_pk_bf16_f32 v141, v150, v151
	v_cvt_pk_bf16_f32 v142, v142, v143
	v_cvt_pk_bf16_f32 v143, v152, v153
	global_store_dwordx4 v[154:155], v[140:143], off offset:3072 sc1
	s_mov_b64 s[26:27], 0
.LBB0_221:
	s_andn2_b64 vcc, exec, s[26:27]
	s_cbranch_vccnz .LBB0_196
	s_lshl_b32 s5, s6, 8
	s_add_i32 s5, s5, s44
	v_readlane_b32 s26, v251, 8
	v_add_u32_e32 v150, s5, v149
	s_lshl_b32 s4, s4, 8
	v_readlane_b32 s27, v251, 9
	s_ashr_i32 s5, s4, 31
	s_movk_i32 s6, 0x3200
	v_mov_b64_e32 v[142:143], s[26:27]
	v_cvt_pk_bf16_f32 v118, v118, v119
	v_cvt_pk_bf16_f32 v119, v120, v121
	v_cvt_pk_bf16_f32 v120, v114, v115
	v_add_u32_e32 v114, 16, v150
	v_cvt_pk_bf16_f32 v102, v102, v103
	v_cvt_pk_bf16_f32 v103, v104, v105
	v_cvt_pk_bf16_f32 v104, v98, v99
	v_add_u32_e32 v98, 32, v150
	v_cvt_pk_bf16_f32 v84, v84, v85
	v_cvt_pk_bf16_f32 v85, v86, v87
	v_cvt_pk_bf16_f32 v86, v80, v81
	v_add_u32_e32 v80, 48, v150
	v_cvt_pk_bf16_f32 v68, v68, v69
	v_cvt_pk_bf16_f32 v69, v70, v71
	v_cvt_pk_bf16_f32 v70, v64, v65
	v_add_u32_e32 v64, 0x80, v150
	v_cvt_pk_bf16_f32 v52, v52, v53
	v_cvt_pk_bf16_f32 v53, v54, v55
	v_cvt_pk_bf16_f32 v54, v48, v49
	v_add_u32_e32 v48, 0x90, v150
	v_cvt_pk_bf16_f32 v36, v36, v37
	v_cvt_pk_bf16_f32 v37, v38, v39
	v_cvt_pk_bf16_f32 v38, v32, v33
	v_add_u32_e32 v32, 0xa0, v150
	v_cvt_pk_bf16_f32 v20, v20, v21
	v_cvt_pk_bf16_f32 v21, v22, v23
	v_cvt_pk_bf16_f32 v22, v16, v17
	v_add_u32_e32 v16, 0xb0, v150
	v_lshlrev_b32_e32 v140, 3, v148
	v_mad_i64_i32 v[148:149], s[26:27], v150, s6, v[142:143]
	s_lshl_b64 s[4:5], s[4:5], 1
	v_mad_i64_i32 v[114:115], s[26:27], v114, s6, v[142:143]
	v_mad_i64_i32 v[98:99], s[26:27], v98, s6, v[142:143]
	v_mad_i64_i32 v[80:81], s[26:27], v80, s6, v[142:143]
	v_mad_i64_i32 v[64:65], s[26:27], v64, s6, v[142:143]
	v_mad_i64_i32 v[48:49], s[26:27], v48, s6, v[142:143]
	v_mad_i64_i32 v[32:33], s[26:27], v32, s6, v[142:143]
	v_mad_i64_i32 v[16:17], s[26:27], v16, s6, v[142:143]
	v_ashrrev_i32_e32 v141, 31, v140
	v_lshl_add_u64 v[148:149], v[148:149], 0, s[4:5]
	v_lshl_add_u64 v[114:115], v[114:115], 0, s[4:5]
	v_lshl_add_u64 v[98:99], v[98:99], 0, s[4:5]
	v_lshl_add_u64 v[80:81], v[80:81], 0, s[4:5]
	v_lshl_add_u64 v[64:65], v[64:65], 0, s[4:5]
	v_lshl_add_u64 v[48:49], v[48:49], 0, s[4:5]
	v_lshl_add_u64 v[32:33], v[32:33], 0, s[4:5]
	v_lshl_add_u64 v[16:17], v[16:17], 0, s[4:5]
	v_lshl_add_u64 v[148:149], v[148:149], 0, s[16:17]
	v_lshlrev_b64 v[140:141], 1, v[140:141]
	v_lshl_add_u64 v[114:115], v[114:115], 0, s[16:17]
	v_lshl_add_u64 v[98:99], v[98:99], 0, s[16:17]
	v_lshl_add_u64 v[80:81], v[80:81], 0, s[16:17]
	v_lshl_add_u64 v[64:65], v[64:65], 0, s[16:17]
	v_lshl_add_u64 v[48:49], v[48:49], 0, s[16:17]
	v_lshl_add_u64 v[32:33], v[32:33], 0, s[16:17]
	v_lshl_add_u64 v[16:17], v[16:17], 0, s[16:17]
	v_lshl_add_u64 v[148:149], v[148:149], 0, v[140:141]
	v_cvt_pk_bf16_f32 v122, v122, v123
	v_cvt_pk_bf16_f32 v123, v124, v125
	v_cvt_pk_bf16_f32 v124, v126, v127
	v_cvt_pk_bf16_f32 v125, v128, v129
	v_cvt_pk_bf16_f32 v121, v116, v117
	v_lshl_add_u64 v[114:115], v[114:115], 0, v[140:141]
	v_cvt_pk_bf16_f32 v110, v110, v111
	v_cvt_pk_bf16_f32 v111, v112, v113
	v_cvt_pk_bf16_f32 v112, v106, v107
	v_cvt_pk_bf16_f32 v113, v108, v109
	v_cvt_pk_bf16_f32 v105, v100, v101
	v_lshl_add_u64 v[98:99], v[98:99], 0, v[140:141]
	v_cvt_pk_bf16_f32 v92, v92, v93
	v_cvt_pk_bf16_f32 v93, v94, v95
	v_cvt_pk_bf16_f32 v94, v88, v89
	v_cvt_pk_bf16_f32 v95, v90, v91
	v_cvt_pk_bf16_f32 v87, v82, v83
	v_lshl_add_u64 v[80:81], v[80:81], 0, v[140:141]
	v_cvt_pk_bf16_f32 v76, v76, v77
	v_cvt_pk_bf16_f32 v77, v78, v79
	v_cvt_pk_bf16_f32 v78, v72, v73
	v_cvt_pk_bf16_f32 v79, v74, v75
	v_cvt_pk_bf16_f32 v71, v66, v67
	v_lshl_add_u64 v[64:65], v[64:65], 0, v[140:141]
	v_cvt_pk_bf16_f32 v60, v60, v61
	v_cvt_pk_bf16_f32 v61, v62, v63
	v_cvt_pk_bf16_f32 v62, v56, v57
	v_cvt_pk_bf16_f32 v63, v58, v59
	v_cvt_pk_bf16_f32 v55, v50, v51
	v_lshl_add_u64 v[48:49], v[48:49], 0, v[140:141]
	v_cvt_pk_bf16_f32 v44, v44, v45
	v_cvt_pk_bf16_f32 v45, v46, v47
	v_cvt_pk_bf16_f32 v46, v40, v41
	v_cvt_pk_bf16_f32 v47, v42, v43
	v_cvt_pk_bf16_f32 v39, v34, v35
	v_lshl_add_u64 v[32:33], v[32:33], 0, v[140:141]
	v_cvt_pk_bf16_f32 v28, v28, v29
	v_cvt_pk_bf16_f32 v29, v30, v31
	v_cvt_pk_bf16_f32 v30, v24, v25
	v_cvt_pk_bf16_f32 v31, v26, v27
	v_cvt_pk_bf16_f32 v23, v18, v19
	v_lshl_add_u64 v[16:17], v[16:17], 0, v[140:141]
	v_cvt_pk_bf16_f32 v12, v12, v13
	v_cvt_pk_bf16_f32 v13, v14, v15
	v_cvt_pk_bf16_f32 v14, v8, v9
	v_cvt_pk_bf16_f32 v15, v10, v11
	v_cvt_pk_bf16_f32 v4, v4, v5
	v_cvt_pk_bf16_f32 v5, v6, v7
	v_cvt_pk_bf16_f32 v6, v0, v1
	v_cvt_pk_bf16_f32 v7, v2, v3
	global_store_dwordx4 v[148:149], v[122:125], off sc1
	global_store_dwordx4 v[148:149], v[118:121], off offset:256 sc1
	global_store_dwordx4 v[114:115], v[110:113], off sc1
	global_store_dwordx4 v[114:115], v[102:105], off offset:256 sc1
	global_store_dwordx4 v[98:99], v[92:95], off sc1
	global_store_dwordx4 v[98:99], v[84:87], off offset:256 sc1
	global_store_dwordx4 v[80:81], v[76:79], off sc1
	global_store_dwordx4 v[80:81], v[68:71], off offset:256 sc1
	global_store_dwordx4 v[64:65], v[60:63], off sc1
	global_store_dwordx4 v[64:65], v[52:55], off offset:256 sc1
	global_store_dwordx4 v[48:49], v[44:47], off sc1
	global_store_dwordx4 v[48:49], v[36:39], off offset:256 sc1
	global_store_dwordx4 v[32:33], v[28:31], off sc1
	global_store_dwordx4 v[32:33], v[20:23], off offset:256 sc1
	global_store_dwordx4 v[16:17], v[12:15], off sc1
	global_store_dwordx4 v[16:17], v[4:7], off offset:256 sc1
	s_branch .LBB0_196

.LBB0_703:
	v_lshlrev_b64 v[68:69], 1, v[68:69]
	s_waitcnt vmcnt(0) lgkmcnt(0)
	v_pk_mul_f32 v[62:63], v[62:63], v[132:133]
	v_pk_mul_f32 v[60:61], v[60:61], v[130:131]
	v_pk_mul_f32 v[74:75], v[58:59], v[66:67]
	v_pk_mul_f32 v[58:59], v[56:57], v[64:65]
	v_lshl_add_u64 v[70:71], v[152:153], 0, v[68:69]
	v_cvt_pk_bf16_f32 v56, v60, v61
	v_cvt_pk_bf16_f32 v57, v62, v63
	v_cvt_pk_bf16_f32 v58, v58, v59
	v_cvt_pk_bf16_f32 v59, v74, v75
	global_store_dwordx4 v[70:71], v[56:59], off sc1
	v_pk_mul_f32 v[54:55], v[54:55], v[132:133]
	v_pk_mul_f32 v[52:53], v[52:53], v[130:131]
	v_pk_mul_f32 v[58:59], v[50:51], v[66:67]
	v_pk_mul_f32 v[50:51], v[48:49], v[64:65]
	v_lshl_add_u64 v[56:57], v[122:123], 0, v[68:69]
	v_cvt_pk_bf16_f32 v48, v52, v53
	v_cvt_pk_bf16_f32 v49, v54, v55
	v_cvt_pk_bf16_f32 v50, v50, v51
	v_cvt_pk_bf16_f32 v51, v58, v59
	global_store_dwordx4 v[56:57], v[48:51], off sc1
	v_pk_mul_f32 v[46:47], v[46:47], v[132:133]
	v_pk_mul_f32 v[44:45], v[44:45], v[130:131]
	v_pk_mul_f32 v[50:51], v[42:43], v[66:67]
	v_pk_mul_f32 v[42:43], v[40:41], v[64:65]
	v_lshl_add_u64 v[48:49], v[114:115], 0, v[68:69]
	v_cvt_pk_bf16_f32 v40, v44, v45
	v_cvt_pk_bf16_f32 v41, v46, v47
	v_cvt_pk_bf16_f32 v42, v42, v43
	v_cvt_pk_bf16_f32 v43, v50, v51
	global_store_dwordx4 v[48:49], v[40:43], off sc1
	v_pk_mul_f32 v[38:39], v[38:39], v[132:133]
	v_pk_mul_f32 v[36:37], v[36:37], v[130:131]
	v_pk_mul_f32 v[42:43], v[34:35], v[66:67]
	v_pk_mul_f32 v[34:35], v[32:33], v[64:65]
	v_lshl_add_u64 v[40:41], v[106:107], 0, v[68:69]
	v_cvt_pk_bf16_f32 v32, v36, v37
	v_cvt_pk_bf16_f32 v33, v38, v39
	v_cvt_pk_bf16_f32 v34, v34, v35
	v_cvt_pk_bf16_f32 v35, v42, v43
	global_store_dwordx4 v[40:41], v[32:35], off sc1
	v_pk_mul_f32 v[30:31], v[30:31], v[132:133]
	v_pk_mul_f32 v[28:29], v[28:29], v[130:131]
	v_pk_mul_f32 v[34:35], v[26:27], v[66:67]
	v_pk_mul_f32 v[26:27], v[24:25], v[64:65]
	v_lshl_add_u64 v[32:33], v[98:99], 0, v[68:69]
	v_cvt_pk_bf16_f32 v24, v28, v29
	v_cvt_pk_bf16_f32 v25, v30, v31
	v_cvt_pk_bf16_f32 v26, v26, v27
	v_cvt_pk_bf16_f32 v27, v34, v35
	global_store_dwordx4 v[32:33], v[24:27], off sc1
	v_pk_mul_f32 v[22:23], v[22:23], v[132:133]
	v_pk_mul_f32 v[20:21], v[20:21], v[130:131]
	v_pk_mul_f32 v[26:27], v[18:19], v[66:67]
	v_pk_mul_f32 v[18:19], v[16:17], v[64:65]
	v_lshl_add_u64 v[24:25], v[88:89], 0, v[68:69]
	v_cvt_pk_bf16_f32 v16, v20, v21
	v_cvt_pk_bf16_f32 v17, v22, v23
	v_cvt_pk_bf16_f32 v18, v18, v19
	v_cvt_pk_bf16_f32 v19, v26, v27
	global_store_dwordx4 v[24:25], v[16:19], off sc1
	v_pk_mul_f32 v[14:15], v[14:15], v[132:133]
	v_pk_mul_f32 v[12:13], v[12:13], v[130:131]
	v_pk_mul_f32 v[18:19], v[10:11], v[66:67]
	v_pk_mul_f32 v[10:11], v[8:9], v[64:65]
	v_lshl_add_u64 v[16:17], v[80:81], 0, v[68:69]
	v_cvt_pk_bf16_f32 v8, v12, v13
	v_cvt_pk_bf16_f32 v9, v14, v15
	v_cvt_pk_bf16_f32 v10, v10, v11
	v_cvt_pk_bf16_f32 v11, v18, v19
	global_store_dwordx4 v[16:17], v[8:11], off sc1
	v_pk_mul_f32 v[6:7], v[6:7], v[132:133]
	v_pk_mul_f32 v[4:5], v[4:5], v[130:131]
	v_pk_mul_f32 v[10:11], v[2:3], v[66:67]
	v_pk_mul_f32 v[2:3], v[0:1], v[64:65]
	v_lshl_add_u64 v[8:9], v[72:73], 0, v[68:69]
	v_cvt_pk_bf16_f32 v0, v4, v5
	v_cvt_pk_bf16_f32 v1, v6, v7
	v_cvt_pk_bf16_f32 v2, v2, v3
	v_cvt_pk_bf16_f32 v3, v10, v11
	s_and_b64 vcc, exec, s[28:29]
	s_mov_b32 s66, s65
	s_mov_b32 s35, s24
	s_mov_b64 s[38:39], s[30:31]
	s_mov_b64 s[2:3], s[26:27]
	global_store_dwordx4 v[8:9], v[0:3], off sc1
	s_cbranch_vccnz .LBB0_716

.LBB0_714:
	s_lshl_b32 s25, s35, 8
	s_add_i32 s25, s25, s53
	v_add_u32_e32 v158, s25, v131
	v_ashrrev_i32_e32 v159, 31, v158
	v_readlane_b32 s4, v253, 10
	v_lshlrev_b64 v[152:153], 11, v[158:159]
	v_readlane_b32 s5, v253, 11
	v_lshlrev_b64 v[160:161], 1, v[150:151]
	s_waitcnt vmcnt(0) lgkmcnt(0)
	v_pk_mul_f32 v[128:129], v[128:129], v[138:139]
	v_lshl_add_u64 v[152:153], s[4:5], 0, v[152:153]
	v_pk_mul_f32 v[126:127], v[126:127], v[136:137]
	v_pk_mul_f32 v[164:165], v[124:125], v[134:135]
	v_pk_mul_f32 v[124:125], v[122:123], v[132:133]
	v_lshl_add_u64 v[162:163], v[152:153], 0, v[160:161]
	v_cvt_pk_bf16_f32 v122, v126, v127
	v_cvt_pk_bf16_f32 v123, v128, v129
	v_cvt_pk_bf16_f32 v124, v124, v125
	v_cvt_pk_bf16_f32 v125, v164, v165
	global_store_dwordx4 v[162:163], v[122:125], off sc1
	v_pk_mul_f32 v[120:121], v[120:121], v[138:139]
	v_pk_mul_f32 v[118:119], v[118:119], v[136:137]
	v_add_u32_e32 v122, 16, v158
	v_ashrrev_i32_e32 v123, 31, v122
	v_lshlrev_b64 v[122:123], 11, v[122:123]
	v_lshl_add_u64 v[122:123], s[4:5], 0, v[122:123]
	v_pk_mul_f32 v[126:127], v[116:117], v[134:135]
	v_pk_mul_f32 v[116:117], v[114:115], v[132:133]
	v_lshl_add_u64 v[124:125], v[122:123], 0, v[160:161]
	v_cvt_pk_bf16_f32 v114, v118, v119
	v_cvt_pk_bf16_f32 v115, v120, v121
	v_cvt_pk_bf16_f32 v116, v116, v117
	v_cvt_pk_bf16_f32 v117, v126, v127
	global_store_dwordx4 v[124:125], v[114:117], off sc1
	v_pk_mul_f32 v[112:113], v[112:113], v[138:139]
	v_pk_mul_f32 v[110:111], v[110:111], v[136:137]
	v_add_u32_e32 v114, 32, v158
	v_ashrrev_i32_e32 v115, 31, v114
	v_lshlrev_b64 v[114:115], 11, v[114:115]
	v_lshl_add_u64 v[114:115], s[4:5], 0, v[114:115]
	v_pk_mul_f32 v[118:119], v[108:109], v[134:135]
	v_pk_mul_f32 v[108:109], v[106:107], v[132:133]
	v_lshl_add_u64 v[116:117], v[114:115], 0, v[160:161]
	v_cvt_pk_bf16_f32 v106, v110, v111
	v_cvt_pk_bf16_f32 v107, v112, v113
	v_cvt_pk_bf16_f32 v108, v108, v109
	v_cvt_pk_bf16_f32 v109, v118, v119
	global_store_dwordx4 v[116:117], v[106:109], off sc1
	v_pk_mul_f32 v[104:105], v[104:105], v[138:139]
	v_pk_mul_f32 v[102:103], v[102:103], v[136:137]
	v_add_u32_e32 v106, 48, v158
	v_ashrrev_i32_e32 v107, 31, v106
	v_lshlrev_b64 v[106:107], 11, v[106:107]
	v_lshl_add_u64 v[106:107], s[4:5], 0, v[106:107]
	v_pk_mul_f32 v[110:111], v[100:101], v[134:135]
	v_pk_mul_f32 v[100:101], v[98:99], v[132:133]
	v_lshl_add_u64 v[108:109], v[106:107], 0, v[160:161]
	v_cvt_pk_bf16_f32 v98, v102, v103
	v_cvt_pk_bf16_f32 v99, v104, v105
	v_cvt_pk_bf16_f32 v100, v100, v101
	v_cvt_pk_bf16_f32 v101, v110, v111
	global_store_dwordx4 v[108:109], v[98:101], off sc1
	v_pk_mul_f32 v[94:95], v[94:95], v[138:139]
	v_pk_mul_f32 v[92:93], v[92:93], v[136:137]
	v_add_u32_e32 v98, 0x80, v158
	v_ashrrev_i32_e32 v99, 31, v98
	v_lshlrev_b64 v[98:99], 11, v[98:99]
	v_lshl_add_u64 v[98:99], s[4:5], 0, v[98:99]
	v_pk_mul_f32 v[102:103], v[90:91], v[134:135]
	v_pk_mul_f32 v[90:91], v[88:89], v[132:133]
	v_lshl_add_u64 v[100:101], v[98:99], 0, v[160:161]
	v_cvt_pk_bf16_f32 v88, v92, v93
	v_cvt_pk_bf16_f32 v89, v94, v95
	v_cvt_pk_bf16_f32 v90, v90, v91
	v_cvt_pk_bf16_f32 v91, v102, v103
	global_store_dwordx4 v[100:101], v[88:91], off sc1
	v_pk_mul_f32 v[86:87], v[86:87], v[138:139]
	v_pk_mul_f32 v[84:85], v[84:85], v[136:137]
	v_add_u32_e32 v88, 0x90, v158
	v_ashrrev_i32_e32 v89, 31, v88
	v_lshlrev_b64 v[88:89], 11, v[88:89]
	v_lshl_add_u64 v[88:89], s[4:5], 0, v[88:89]
	v_pk_mul_f32 v[92:93], v[82:83], v[134:135]
	v_pk_mul_f32 v[82:83], v[80:81], v[132:133]
	v_lshl_add_u64 v[90:91], v[88:89], 0, v[160:161]
	v_cvt_pk_bf16_f32 v80, v84, v85
	v_cvt_pk_bf16_f32 v81, v86, v87
	v_cvt_pk_bf16_f32 v82, v82, v83
	v_cvt_pk_bf16_f32 v83, v92, v93
	global_store_dwordx4 v[90:91], v[80:83], off sc1
	v_pk_mul_f32 v[78:79], v[78:79], v[138:139]
	v_pk_mul_f32 v[76:77], v[76:77], v[136:137]
	v_add_u32_e32 v80, 0xa0, v158
	v_ashrrev_i32_e32 v81, 31, v80
	v_lshlrev_b64 v[80:81], 11, v[80:81]
	v_lshl_add_u64 v[80:81], s[4:5], 0, v[80:81]
	v_pk_mul_f32 v[84:85], v[74:75], v[134:135]
	v_pk_mul_f32 v[74:75], v[72:73], v[132:133]
	v_lshl_add_u64 v[82:83], v[80:81], 0, v[160:161]
	v_cvt_pk_bf16_f32 v72, v76, v77
	v_cvt_pk_bf16_f32 v73, v78, v79
	v_cvt_pk_bf16_f32 v74, v74, v75
	v_cvt_pk_bf16_f32 v75, v84, v85
	global_store_dwordx4 v[82:83], v[72:75], off sc1
	v_pk_mul_f32 v[70:71], v[70:71], v[138:139]
	v_pk_mul_f32 v[68:69], v[68:69], v[136:137]
	v_add_u32_e32 v72, 0xb0, v158
	v_ashrrev_i32_e32 v73, 31, v72
	v_lshlrev_b64 v[72:73], 11, v[72:73]
	v_lshl_add_u64 v[72:73], s[4:5], 0, v[72:73]
	v_pk_mul_f32 v[76:77], v[66:67], v[134:135]
	v_pk_mul_f32 v[66:67], v[64:65], v[132:133]
	v_lshl_add_u64 v[74:75], v[72:73], 0, v[160:161]
	v_cvt_pk_bf16_f32 v64, v68, v69
	v_cvt_pk_bf16_f32 v65, v70, v71
	v_cvt_pk_bf16_f32 v66, v66, v67
	v_cvt_pk_bf16_f32 v67, v76, v77
	v_add_u32_e32 v68, 0x80, v150
	global_store_dwordx4 v[74:75], v[64:67], off sc1
	v_ashrrev_i32_e32 v69, 31, v68
	s_and_b64 vcc, exec, s[2:3]
	v_mov_b32_e32 v131, 1.0
	v_mov_b32_e32 v132, 1.0
	v_mov_b32_e32 v133, 1.0
	v_mov_b32_e32 v64, 1.0
	v_mov_b32_e32 v65, 1.0
	v_mov_b32_e32 v66, 1.0
	v_mov_b32_e32 v67, 1.0
	s_cbranch_vccnz .LBB0_703
	v_lshl_add_u64 v[64:65], v[68:69], 2, s[18:19]
	flat_load_dwordx4 v[130:133], v[64:65]
	s_nop 0
	flat_load_dwordx4 v[64:67], v[64:65] offset:16
	s_branch .LBB0_703

.LBB0_1004:
	v_pk_mul_f32 v[116:117], v[116:117], v[152:153]
	s_cmp_eq_u32 s21, 2
	v_lshlrev_b32_e32 v152, 3, v96
	v_pk_mul_f32 v[118:119], v[118:119], v[154:155]
	s_cselect_b64 s[24:25], -1, 0
	v_add_u32_e32 v154, s51, v192
	v_ashrrev_i32_e32 v153, 31, v152
	v_pk_mul_f32 v[122:123], v[122:123], v[186:187]
	v_pk_mul_f32 v[120:121], v[120:121], v[184:185]
	v_pk_mul_f32 v[94:95], v[94:95], v[182:183]
	v_pk_mul_f32 v[92:93], v[92:93], v[180:181]
	v_pk_mul_f32 v[90:91], v[90:91], v[158:159]
	v_pk_mul_f32 v[88:89], v[88:89], v[156:157]
	v_pk_mul_f32 v[130:131], v[130:131], v[178:179]
	v_pk_mul_f32 v[128:129], v[128:129], v[176:177]
	v_pk_mul_f32 v[126:127], v[126:127], v[162:163]
	v_pk_mul_f32 v[124:125], v[124:125], v[160:161]
	v_pk_mul_f32 v[86:87], v[86:87], v[190:191]
	v_pk_mul_f32 v[84:85], v[84:85], v[188:189]
	v_pk_mul_f32 v[82:83], v[82:83], v[150:151]
	v_pk_mul_f32 v[80:81], v[80:81], v[148:149]
	s_and_b64 vcc, exec, s[24:25]
	v_lshlrev_b64 v[176:177], 1, v[152:153]
	v_lshl_add_u32 v178, s20, 8, v154
	s_cbranch_vccz .LBB0_1006
	v_ashrrev_i32_e32 v179, 31, v178
	v_readlane_b32 s40, v253, 34
	s_lshl_b32 s20, s59, 8
	v_lshlrev_b64 v[148:149], 12, v[178:179]
	v_readlane_b32 s41, v253, 35
	s_ashr_i32 s21, s20, 31
	s_lshl_b64 s[20:21], s[20:21], 1
	v_lshl_add_u64 v[148:149], s[40:41], 0, v[148:149]
	v_lshl_add_u64 v[148:149], v[148:149], 0, s[20:21]
	s_lshl_b32 s26, s52, 1
	s_mov_b32 s27, s17
	v_lshl_add_u64 v[148:149], v[148:149], 0, s[26:27]
	v_lshl_add_u64 v[152:153], v[148:149], 0, v[176:177]
	v_cvt_pk_bf16_f32 v148, v128, v129
	v_cvt_pk_bf16_f32 v149, v130, v131
	v_cvt_pk_bf16_f32 v150, v124, v125
	v_cvt_pk_bf16_f32 v151, v126, v127
	global_store_dwordx4 v[152:153], v[148:151], off sc1
	s_nop 1
	v_cvt_pk_bf16_f32 v148, v92, v93
	v_cvt_pk_bf16_f32 v149, v94, v95
	v_cvt_pk_bf16_f32 v150, v88, v89
	v_cvt_pk_bf16_f32 v151, v90, v91
	global_store_dwordx4 v[152:153], v[148:151], off offset:256 sc1
	s_nop 1
	v_add_u32_e32 v148, 16, v178
	v_ashrrev_i32_e32 v149, 31, v148
	v_lshlrev_b64 v[148:149], 12, v[148:149]
	v_lshl_add_u64 v[148:149], s[40:41], 0, v[148:149]
	v_lshl_add_u64 v[148:149], v[148:149], 0, s[20:21]
	v_lshl_add_u64 v[148:149], v[148:149], 0, s[26:27]
	v_lshl_add_u64 v[152:153], v[148:149], 0, v[176:177]
	v_cvt_pk_bf16_f32 v148, v120, v121
	v_cvt_pk_bf16_f32 v149, v122, v123
	v_cvt_pk_bf16_f32 v150, v116, v117
	v_cvt_pk_bf16_f32 v151, v118, v119
	global_store_dwordx4 v[152:153], v[148:151], off sc1
	s_nop 1
	v_cvt_pk_bf16_f32 v148, v84, v85
	v_cvt_pk_bf16_f32 v149, v86, v87
	v_cvt_pk_bf16_f32 v150, v80, v81
	v_cvt_pk_bf16_f32 v151, v82, v83
	global_store_dwordx4 v[152:153], v[148:151], off offset:256 sc1

.LBB0_1024:
	v_cndmask_b32_e64 v96, 0, 1, s[24:25]
	v_pk_mul_f32 v[106:107], v[106:107], v[190:191]
	v_pk_mul_f32 v[104:105], v[104:105], v[188:189]
	v_pk_mul_f32 v[102:103], v[102:103], v[154:155]
	v_pk_mul_f32 v[100:101], v[100:101], v[152:153]
	v_pk_mul_f32 v[78:79], v[78:79], v[186:187]
	v_pk_mul_f32 v[76:77], v[76:77], v[184:185]
	v_pk_mul_f32 v[74:75], v[74:75], v[158:159]
	v_pk_mul_f32 v[72:73], v[72:73], v[156:157]
	v_pk_mul_f32 v[114:115], v[114:115], v[182:183]
	v_pk_mul_f32 v[112:113], v[112:113], v[180:181]
	v_pk_mul_f32 v[110:111], v[110:111], v[162:163]
	v_pk_mul_f32 v[108:109], v[108:109], v[160:161]
	v_pk_mul_f32 v[70:71], v[70:71], v[194:195]
	v_pk_mul_f32 v[68:69], v[68:69], v[192:193]
	v_pk_mul_f32 v[66:67], v[66:67], v[150:151]
	v_cmp_ne_u32_e64 s[42:43], 1, v96
	s_andn2_b64 vcc, exec, s[24:25]
	v_pk_mul_f32 v[64:65], v[64:65], v[148:149]
	s_cbranch_vccnz .LBB0_1026
	v_add_u32_e32 v148, 32, v178
	v_ashrrev_i32_e32 v149, 31, v148
	v_readlane_b32 s24, v253, 34
	s_lshl_b32 s20, s59, 8
	v_lshlrev_b64 v[148:149], 12, v[148:149]
	v_readlane_b32 s25, v253, 35
	s_ashr_i32 s21, s20, 31
	s_lshl_b64 s[20:21], s[20:21], 1
	v_lshl_add_u64 v[148:149], s[24:25], 0, v[148:149]
	v_lshl_add_u64 v[148:149], v[148:149], 0, s[20:21]
	s_lshl_b32 s22, s52, 1
	s_mov_b32 s23, s17
	v_lshl_add_u64 v[148:149], v[148:149], 0, s[22:23]
	v_lshl_add_u64 v[152:153], v[148:149], 0, v[176:177]
	v_cvt_pk_bf16_f32 v148, v112, v113
	v_cvt_pk_bf16_f32 v149, v114, v115
	v_cvt_pk_bf16_f32 v150, v108, v109
	v_cvt_pk_bf16_f32 v151, v110, v111
	global_store_dwordx4 v[152:153], v[148:151], off sc1
	s_nop 1
	v_cvt_pk_bf16_f32 v148, v76, v77
	v_cvt_pk_bf16_f32 v149, v78, v79
	v_cvt_pk_bf16_f32 v150, v72, v73
	v_cvt_pk_bf16_f32 v151, v74, v75
	global_store_dwordx4 v[152:153], v[148:151], off offset:256 sc1
	s_nop 1
	v_add_u32_e32 v148, 48, v178
	v_ashrrev_i32_e32 v149, 31, v148
	v_lshlrev_b64 v[148:149], 12, v[148:149]
	v_lshl_add_u64 v[148:149], s[24:25], 0, v[148:149]
	v_lshl_add_u64 v[148:149], v[148:149], 0, s[20:21]
	v_lshl_add_u64 v[148:149], v[148:149], 0, s[22:23]
	v_lshl_add_u64 v[152:153], v[148:149], 0, v[176:177]
	v_cvt_pk_bf16_f32 v148, v104, v105
	v_cvt_pk_bf16_f32 v149, v106, v107
	v_cvt_pk_bf16_f32 v150, v100, v101
	v_cvt_pk_bf16_f32 v151, v102, v103
	global_store_dwordx4 v[152:153], v[148:151], off sc1
	s_nop 1
	v_cvt_pk_bf16_f32 v148, v68, v69
	v_cvt_pk_bf16_f32 v149, v70, v71
	v_cvt_pk_bf16_f32 v150, v64, v65
	v_cvt_pk_bf16_f32 v151, v66, v67
	global_store_dwordx4 v[152:153], v[148:151], off offset:256 sc1

.LBB0_1044:
	v_pk_mul_f32 v[54:55], v[54:55], v[190:191]
	v_pk_mul_f32 v[52:53], v[52:53], v[188:189]
	v_pk_mul_f32 v[50:51], v[50:51], v[154:155]
	v_pk_mul_f32 v[48:49], v[48:49], v[152:153]
	v_pk_mul_f32 v[30:31], v[30:31], v[186:187]
	v_pk_mul_f32 v[28:29], v[28:29], v[184:185]
	v_pk_mul_f32 v[26:27], v[26:27], v[158:159]
	v_pk_mul_f32 v[24:25], v[24:25], v[156:157]
	v_pk_mul_f32 v[62:63], v[62:63], v[182:183]
	v_pk_mul_f32 v[60:61], v[60:61], v[180:181]
	v_pk_mul_f32 v[58:59], v[58:59], v[162:163]
	v_pk_mul_f32 v[56:57], v[56:57], v[160:161]
	v_pk_mul_f32 v[22:23], v[22:23], v[194:195]
	v_pk_mul_f32 v[20:21], v[20:21], v[192:193]
	v_pk_mul_f32 v[18:19], v[18:19], v[150:151]
	s_and_b64 vcc, exec, s[42:43]
	v_pk_mul_f32 v[16:17], v[16:17], v[148:149]
	s_cbranch_vccnz .LBB0_1046
	v_add_u32_e32 v148, 0x80, v178
	v_ashrrev_i32_e32 v149, 31, v148
	v_readlane_b32 s24, v253, 34
	s_lshl_b32 s20, s59, 8
	v_lshlrev_b64 v[148:149], 12, v[148:149]
	v_readlane_b32 s25, v253, 35
	s_ashr_i32 s21, s20, 31
	s_lshl_b64 s[20:21], s[20:21], 1
	v_lshl_add_u64 v[148:149], s[24:25], 0, v[148:149]
	v_lshl_add_u64 v[148:149], v[148:149], 0, s[20:21]
	s_lshl_b32 s22, s52, 1
	s_mov_b32 s23, s17
	v_lshl_add_u64 v[148:149], v[148:149], 0, s[22:23]
	v_lshl_add_u64 v[152:153], v[148:149], 0, v[176:177]
	v_cvt_pk_bf16_f32 v148, v60, v61
	v_cvt_pk_bf16_f32 v149, v62, v63
	v_cvt_pk_bf16_f32 v150, v56, v57
	v_cvt_pk_bf16_f32 v151, v58, v59
	global_store_dwordx4 v[152:153], v[148:151], off sc1
	s_nop 1
	v_cvt_pk_bf16_f32 v148, v28, v29
	v_cvt_pk_bf16_f32 v149, v30, v31
	v_cvt_pk_bf16_f32 v150, v24, v25
	v_cvt_pk_bf16_f32 v151, v26, v27
	global_store_dwordx4 v[152:153], v[148:151], off offset:256 sc1
	s_nop 1
	v_add_u32_e32 v148, 0x90, v178
	v_ashrrev_i32_e32 v149, 31, v148
	v_lshlrev_b64 v[148:149], 12, v[148:149]
	v_lshl_add_u64 v[148:149], s[24:25], 0, v[148:149]
	v_lshl_add_u64 v[148:149], v[148:149], 0, s[20:21]
	v_lshl_add_u64 v[148:149], v[148:149], 0, s[22:23]
	v_lshl_add_u64 v[152:153], v[148:149], 0, v[176:177]
	v_cvt_pk_bf16_f32 v148, v52, v53
	v_cvt_pk_bf16_f32 v149, v54, v55
	v_cvt_pk_bf16_f32 v150, v48, v49
	v_cvt_pk_bf16_f32 v151, v50, v51
	global_store_dwordx4 v[152:153], v[148:151], off sc1
	s_nop 1
	v_cvt_pk_bf16_f32 v148, v20, v21
	v_cvt_pk_bf16_f32 v149, v22, v23
	v_cvt_pk_bf16_f32 v150, v16, v17
	v_cvt_pk_bf16_f32 v151, v18, v19
	global_store_dwordx4 v[152:153], v[148:151], off offset:256 sc1

.LBB0_1064:
	v_pk_mul_f32 v[38:39], v[38:39], v[154:155]
	v_pk_mul_f32 v[36:37], v[36:37], v[152:153]
	v_pk_mul_f32 v[34:35], v[34:35], v[142:143]
	v_pk_mul_f32 v[32:33], v[32:33], v[140:141]
	v_pk_mul_f32 v[14:15], v[14:15], v[158:159]
	v_pk_mul_f32 v[12:13], v[12:13], v[156:157]
	v_pk_mul_f32 v[10:11], v[10:11], v[146:147]
	v_pk_mul_f32 v[8:9], v[8:9], v[144:145]
	v_pk_mul_f32 v[46:47], v[46:47], v[180:181]
	v_pk_mul_f32 v[44:45], v[44:45], v[162:163]
	v_pk_mul_f32 v[42:43], v[42:43], v[160:161]
	v_pk_mul_f32 v[40:41], v[40:41], v[98:99]
	v_pk_mul_f32 v[6:7], v[6:7], v[150:151]
	v_pk_mul_f32 v[4:5], v[4:5], v[148:149]
	v_pk_mul_f32 v[2:3], v[2:3], v[138:139]
	s_and_b64 vcc, exec, s[42:43]
	v_pk_mul_f32 v[0:1], v[0:1], v[136:137]
	s_cbranch_vccnz .LBB0_1066
	v_add_u32_e32 v98, 0xa0, v178
	v_ashrrev_i32_e32 v99, 31, v98
	v_readlane_b32 s24, v253, 34
	s_lshl_b32 s20, s59, 8
	v_lshlrev_b64 v[98:99], 12, v[98:99]
	v_readlane_b32 s25, v253, 35
	s_ashr_i32 s21, s20, 31
	s_lshl_b64 s[20:21], s[20:21], 1
	v_lshl_add_u64 v[98:99], s[24:25], 0, v[98:99]
	v_lshl_add_u64 v[98:99], v[98:99], 0, s[20:21]
	s_lshl_b32 s22, s52, 1
	s_mov_b32 s23, s17
	v_lshl_add_u64 v[98:99], v[98:99], 0, s[22:23]
	v_lshl_add_u64 v[98:99], v[98:99], 0, v[176:177]
	v_cvt_pk_bf16_f32 v132, v44, v45
	v_cvt_pk_bf16_f32 v133, v46, v47
	v_cvt_pk_bf16_f32 v134, v40, v41
	v_cvt_pk_bf16_f32 v135, v42, v43
	global_store_dwordx4 v[98:99], v[132:135], off sc1
	s_nop 1
	v_cvt_pk_bf16_f32 v132, v12, v13
	v_cvt_pk_bf16_f32 v133, v14, v15
	v_cvt_pk_bf16_f32 v134, v8, v9
	v_cvt_pk_bf16_f32 v135, v10, v11
	global_store_dwordx4 v[98:99], v[132:135], off offset:256 sc1
	v_add_u32_e32 v98, 0xb0, v178
	v_ashrrev_i32_e32 v99, 31, v98
	v_lshlrev_b64 v[98:99], 12, v[98:99]
	v_lshl_add_u64 v[98:99], s[24:25], 0, v[98:99]
	v_lshl_add_u64 v[98:99], v[98:99], 0, s[20:21]
	v_lshl_add_u64 v[98:99], v[98:99], 0, s[22:23]
	v_lshl_add_u64 v[98:99], v[98:99], 0, v[176:177]
	v_cvt_pk_bf16_f32 v132, v36, v37
	v_cvt_pk_bf16_f32 v133, v38, v39
	v_cvt_pk_bf16_f32 v134, v32, v33
	v_cvt_pk_bf16_f32 v135, v34, v35
	global_store_dwordx4 v[98:99], v[132:135], off sc1
	s_nop 1
	v_cvt_pk_bf16_f32 v132, v4, v5
	v_cvt_pk_bf16_f32 v133, v6, v7
	v_cvt_pk_bf16_f32 v134, v0, v1
	v_cvt_pk_bf16_f32 v135, v2, v3
	global_store_dwordx4 v[98:99], v[132:135], off offset:256 sc1

.LBB0_1148:
	v_mov_b32_e32 v146, v140
	v_mov_b32_e32 v144, v141
	s_lshl_b32 s2, s2, 8
	s_add_i32 s2, s2, s35
	s_add_i32 s14, s45, s40
	v_add_u32_e32 v146, s2, v146
	v_lshl_add_u32 v144, v144, 3, s14
	v_ashrrev_i32_e32 v147, 31, v146
	v_readlane_b32 s14, v252, 28
	v_ashrrev_i32_e32 v145, 31, v144
	v_lshlrev_b64 v[148:149], 12, v[146:147]
	v_readlane_b32 s15, v252, 29
	v_lshlrev_b64 v[150:151], 1, v[144:145]
	v_cvt_pk_bf16_f32 v122, v122, v123
	v_lshl_add_u64 v[148:149], s[14:15], 0, v[148:149]
	v_lshl_add_u64 v[152:153], v[148:149], 0, v[150:151]
	v_cvt_pk_bf16_f32 v123, v124, v125
	v_cvt_pk_bf16_f32 v124, v126, v127
	v_cvt_pk_bf16_f32 v125, v128, v129
	global_store_dwordx4 v[152:153], v[122:125], off sc1
	v_cvt_pk_bf16_f32 v118, v118, v119
	v_cvt_pk_bf16_f32 v119, v120, v121
	v_add_u32_e32 v122, 16, v146
	v_cvt_pk_bf16_f32 v120, v114, v115
	v_add_u32_e32 v114, 32, v146
	v_cvt_pk_bf16_f32 v110, v110, v111
	v_cvt_pk_bf16_f32 v111, v112, v113
	v_cvt_pk_bf16_f32 v112, v106, v107
	v_add_u32_e32 v106, 48, v146
	v_cvt_pk_bf16_f32 v102, v102, v103
	v_cvt_pk_bf16_f32 v103, v104, v105
	v_cvt_pk_bf16_f32 v104, v98, v99
	v_add_u32_e32 v98, 0x80, v146
	v_cvt_pk_bf16_f32 v92, v92, v93
	v_cvt_pk_bf16_f32 v93, v94, v95
	v_cvt_pk_bf16_f32 v94, v88, v89
	v_add_u32_e32 v88, 0x90, v146
	v_cvt_pk_bf16_f32 v84, v84, v85
	v_cvt_pk_bf16_f32 v85, v86, v87
	v_cvt_pk_bf16_f32 v86, v80, v81
	v_add_u32_e32 v80, 0xa0, v146
	v_cvt_pk_bf16_f32 v76, v76, v77
	v_cvt_pk_bf16_f32 v77, v78, v79
	v_cvt_pk_bf16_f32 v78, v72, v73
	v_add_u32_e32 v72, 0xb0, v146
	v_ashrrev_i32_e32 v123, 31, v122
	v_ashrrev_i32_e32 v115, 31, v114
	v_ashrrev_i32_e32 v107, 31, v106
	v_ashrrev_i32_e32 v99, 31, v98
	v_ashrrev_i32_e32 v89, 31, v88
	v_ashrrev_i32_e32 v81, 31, v80
	v_ashrrev_i32_e32 v73, 31, v72
	v_cvt_pk_bf16_f32 v68, v68, v69
	v_cvt_pk_bf16_f32 v69, v70, v71
	v_cvt_pk_bf16_f32 v70, v64, v65
	v_add_u32_e32 v64, 0x80, v144
	v_lshlrev_b64 v[122:123], 12, v[122:123]
	v_lshlrev_b64 v[114:115], 12, v[114:115]
	v_lshlrev_b64 v[106:107], 12, v[106:107]
	v_lshlrev_b64 v[98:99], 12, v[98:99]
	v_lshlrev_b64 v[88:89], 12, v[88:89]
	v_lshlrev_b64 v[80:81], 12, v[80:81]
	v_lshlrev_b64 v[72:73], 12, v[72:73]
	v_ashrrev_i32_e32 v65, 31, v64
	v_lshl_add_u64 v[122:123], s[14:15], 0, v[122:123]
	v_lshl_add_u64 v[114:115], s[14:15], 0, v[114:115]
	v_lshl_add_u64 v[106:107], s[14:15], 0, v[106:107]
	v_lshl_add_u64 v[98:99], s[14:15], 0, v[98:99]
	v_lshl_add_u64 v[88:89], s[14:15], 0, v[88:89]
	v_lshl_add_u64 v[80:81], s[14:15], 0, v[80:81]
	v_lshl_add_u64 v[72:73], s[14:15], 0, v[72:73]
	v_lshlrev_b64 v[64:65], 1, v[64:65]
	v_lshl_add_u64 v[124:125], v[122:123], 0, v[150:151]
	v_cvt_pk_bf16_f32 v121, v116, v117
	v_lshl_add_u64 v[116:117], v[114:115], 0, v[150:151]
	v_cvt_pk_bf16_f32 v113, v108, v109
	v_lshl_add_u64 v[108:109], v[106:107], 0, v[150:151]
	v_cvt_pk_bf16_f32 v105, v100, v101
	v_lshl_add_u64 v[100:101], v[98:99], 0, v[150:151]
	v_cvt_pk_bf16_f32 v95, v90, v91
	v_lshl_add_u64 v[90:91], v[88:89], 0, v[150:151]
	v_cvt_pk_bf16_f32 v87, v82, v83
	v_lshl_add_u64 v[82:83], v[80:81], 0, v[150:151]
	v_cvt_pk_bf16_f32 v79, v74, v75
	v_lshl_add_u64 v[74:75], v[72:73], 0, v[150:151]
	v_cvt_pk_bf16_f32 v71, v66, v67
	v_lshl_add_u64 v[66:67], v[148:149], 0, v[64:65]
	v_cvt_pk_bf16_f32 v60, v60, v61
	v_cvt_pk_bf16_f32 v61, v62, v63
	v_cvt_pk_bf16_f32 v62, v56, v57
	v_cvt_pk_bf16_f32 v63, v58, v59
	v_lshl_add_u64 v[56:57], v[122:123], 0, v[64:65]
	v_cvt_pk_bf16_f32 v52, v52, v53
	v_cvt_pk_bf16_f32 v53, v54, v55
	v_cvt_pk_bf16_f32 v54, v48, v49
	v_cvt_pk_bf16_f32 v55, v50, v51
	v_lshl_add_u64 v[48:49], v[114:115], 0, v[64:65]
	v_cvt_pk_bf16_f32 v44, v44, v45
	v_cvt_pk_bf16_f32 v45, v46, v47
	v_cvt_pk_bf16_f32 v46, v40, v41
	v_cvt_pk_bf16_f32 v47, v42, v43
	v_lshl_add_u64 v[40:41], v[106:107], 0, v[64:65]
	v_cvt_pk_bf16_f32 v36, v36, v37
	v_cvt_pk_bf16_f32 v37, v38, v39
	v_cvt_pk_bf16_f32 v38, v32, v33
	v_cvt_pk_bf16_f32 v39, v34, v35
	v_lshl_add_u64 v[32:33], v[98:99], 0, v[64:65]
	v_cvt_pk_bf16_f32 v28, v28, v29
	v_cvt_pk_bf16_f32 v29, v30, v31
	v_cvt_pk_bf16_f32 v30, v24, v25
	v_cvt_pk_bf16_f32 v31, v26, v27
	v_lshl_add_u64 v[24:25], v[88:89], 0, v[64:65]
	v_cvt_pk_bf16_f32 v20, v20, v21
	v_cvt_pk_bf16_f32 v21, v22, v23
	v_cvt_pk_bf16_f32 v22, v16, v17
	v_cvt_pk_bf16_f32 v23, v18, v19
	v_lshl_add_u64 v[16:17], v[80:81], 0, v[64:65]
	v_cvt_pk_bf16_f32 v12, v12, v13
	v_cvt_pk_bf16_f32 v13, v14, v15
	v_cvt_pk_bf16_f32 v14, v8, v9
	v_cvt_pk_bf16_f32 v15, v10, v11
	v_lshl_add_u64 v[8:9], v[72:73], 0, v[64:65]
	v_cvt_pk_bf16_f32 v4, v4, v5
	v_cvt_pk_bf16_f32 v5, v6, v7
	v_cvt_pk_bf16_f32 v6, v0, v1
	v_cvt_pk_bf16_f32 v7, v2, v3
	s_and_b64 vcc, exec, s[6:7]
	s_mov_b32 s45, s9
	s_mov_b32 s2, s8
	s_mov_b64 s[18:19], s[12:13]
	s_mov_b64 s[14:15], s[10:11]
	global_store_dwordx4 v[124:125], v[118:121], off sc1
	global_store_dwordx4 v[116:117], v[110:113], off sc1
	global_store_dwordx4 v[108:109], v[102:105], off sc1
	global_store_dwordx4 v[100:101], v[92:95], off sc1
	global_store_dwordx4 v[90:91], v[84:87], off sc1
	global_store_dwordx4 v[82:83], v[76:79], off sc1
	global_store_dwordx4 v[74:75], v[68:71], off sc1
	global_store_dwordx4 v[66:67], v[60:63], off sc1
	global_store_dwordx4 v[56:57], v[52:55], off sc1
	global_store_dwordx4 v[48:49], v[44:47], off sc1
	global_store_dwordx4 v[40:41], v[36:39], off sc1
	global_store_dwordx4 v[32:33], v[28:31], off sc1
	global_store_dwordx4 v[24:25], v[20:23], off sc1
	global_store_dwordx4 v[16:17], v[12:15], off sc1
	global_store_dwordx4 v[8:9], v[4:7], off sc1
	s_cbranch_vccnz .LBB0_1156

.LBB0_1519:
	v_mov_b32_e32 v96, v149
	v_mov_b32_e32 v138, v148
	s_lshl_b32 s5, s12, 8
	v_lshlrev_b32_e32 v140, 3, v96
	v_mul_f32_e32 v96, 0xbfb8aa3b, v126
	v_exp_f32_e32 v142, v96
	v_mul_f32_e32 v96, 0xbfb8aa3b, v127
	v_exp_f32_e32 v143, v96
	s_add_i32 s5, s5, s44
	v_add_u32_e32 v138, s5, v138
	s_lshl_b32 s12, s50, 7
	v_pk_add_f32 v[142:143], v[142:143], 1.0 op_sel_hi:[1,0]
	v_readlane_b32 s18, v253, 52
	v_div_scale_f32 v96, s[14:15], v143, v143, v127
	v_rcp_f32_e32 v139, v96
	s_ashr_i32 s13, s12, 31
	v_readlane_b32 s19, v253, 53
	s_lshl_b64 s[12:13], s[12:13], 1
	v_fma_f32 v144, -v96, v139, 1.0
	v_fmac_f32_e32 v139, v144, v139
	v_div_scale_f32 v144, vcc, v127, v143, v127
	v_mul_f32_e32 v145, v144, v139
	v_fma_f32 v156, -v96, v145, v144
	v_fmac_f32_e32 v145, v156, v139
	v_fma_f32 v96, -v96, v145, v144
	v_div_fmas_f32 v96, v96, v139, v145
	v_div_fixup_f32 v127, v96, v143, v127
	v_div_scale_f32 v96, s[14:15], v142, v142, v126
	v_rcp_f32_e32 v139, v96
	v_ashrrev_i32_e32 v141, 31, v140
	s_mov_b32 s50, s49
	v_fma_f32 v143, -v96, v139, 1.0
	v_fmac_f32_e32 v139, v143, v139
	v_div_scale_f32 v143, vcc, v126, v142, v126
	v_mul_f32_e32 v144, v143, v139
	v_fma_f32 v145, -v96, v144, v143
	v_fmac_f32_e32 v144, v145, v139
	v_fma_f32 v96, -v96, v144, v143
	v_div_fmas_f32 v96, v96, v139, v144
	v_div_fixup_f32 v126, v96, v142, v126
	v_mul_f32_e32 v96, 0xbfb8aa3b, v128
	v_pk_mul_f32 v[122:123], v[122:123], v[126:127]
	v_exp_f32_e32 v126, v96
	v_mul_f32_e32 v96, 0xbfb8aa3b, v129
	v_exp_f32_e32 v127, v96
	s_nop 0
	v_pk_add_f32 v[126:127], v[126:127], 1.0 op_sel_hi:[1,0]
	s_nop 0
	v_div_scale_f32 v96, s[14:15], v127, v127, v129
	v_rcp_f32_e32 v139, v96
	s_nop 0
	v_fma_f32 v142, -v96, v139, 1.0
	v_fmac_f32_e32 v139, v142, v139
	v_div_scale_f32 v142, vcc, v129, v127, v129
	v_mul_f32_e32 v143, v142, v139
	v_fma_f32 v144, -v96, v143, v142
	v_fmac_f32_e32 v143, v144, v139
	v_fma_f32 v96, -v96, v143, v142
	v_div_fmas_f32 v96, v96, v139, v143
	v_div_fixup_f32 v127, v96, v127, v129
	v_div_scale_f32 v96, s[14:15], v126, v126, v128
	v_rcp_f32_e32 v129, v96
	v_mov_b32_e32 v144, v155
	v_fma_f32 v139, -v96, v129, 1.0
	v_fmac_f32_e32 v129, v139, v129
	v_div_scale_f32 v139, vcc, v128, v126, v128
	v_mul_f32_e32 v142, v139, v129
	v_fma_f32 v143, -v96, v142, v139
	v_fmac_f32_e32 v142, v143, v129
	v_fma_f32 v96, -v96, v142, v139
	v_div_fmas_f32 v96, v96, v129, v142
	v_div_fixup_f32 v126, v96, v126, v128
	v_mul_f32_e32 v96, 0xbfb8aa3b, v118
	v_pk_mul_f32 v[124:125], v[124:125], v[126:127]
	v_exp_f32_e32 v126, v96
	v_mul_f32_e32 v96, 0xbfb8aa3b, v119
	v_exp_f32_e32 v127, v96
	s_nop 0
	v_pk_add_f32 v[126:127], v[126:127], 1.0 op_sel_hi:[1,0]
	s_nop 0
	v_div_scale_f32 v96, s[14:15], v127, v127, v119
	v_rcp_f32_e32 v128, v96
	s_nop 0
	v_fma_f32 v129, -v96, v128, 1.0
	v_fmac_f32_e32 v128, v129, v128
	v_div_scale_f32 v129, vcc, v119, v127, v119
	v_mul_f32_e32 v139, v129, v128
	v_fma_f32 v142, -v96, v139, v129
	v_fmac_f32_e32 v139, v142, v128
	v_fma_f32 v96, -v96, v139, v129
	v_div_fmas_f32 v96, v96, v128, v139
	v_div_fixup_f32 v119, v96, v127, v119
	v_div_scale_f32 v96, s[14:15], v126, v126, v118
	v_rcp_f32_e32 v127, v96
	v_mov_b32_e32 v142, v154
	v_fma_f32 v128, -v96, v127, 1.0
	v_fmac_f32_e32 v127, v128, v127
	v_div_scale_f32 v128, vcc, v118, v126, v118
	v_mul_f32_e32 v129, v128, v127
	v_fma_f32 v139, -v96, v129, v128
	v_fmac_f32_e32 v129, v139, v127
	v_fma_f32 v96, -v96, v129, v128
	v_div_fmas_f32 v96, v96, v127, v129
	v_div_fixup_f32 v118, v96, v126, v118
	v_mul_f32_e32 v96, 0xbfb8aa3b, v120
	v_pk_mul_f32 v[118:119], v[114:115], v[118:119]
	v_exp_f32_e32 v114, v96
	v_mul_f32_e32 v96, 0xbfb8aa3b, v121
	v_exp_f32_e32 v115, v96
	v_ashrrev_i32_e32 v139, 31, v138
	v_cvt_pk_bf16_f32 v118, v118, v119
	v_pk_add_f32 v[114:115], v[114:115], 1.0 op_sel_hi:[1,0]
	s_nop 0
	v_div_scale_f32 v96, s[14:15], v115, v115, v121
	v_rcp_f32_e32 v126, v96
	s_nop 0
	v_fma_f32 v127, -v96, v126, 1.0
	v_fmac_f32_e32 v126, v127, v126
	v_div_scale_f32 v127, vcc, v121, v115, v121
	v_mul_f32_e32 v128, v127, v126
	v_fma_f32 v129, -v96, v128, v127
	v_fmac_f32_e32 v128, v129, v126
	v_fma_f32 v96, -v96, v128, v127
	v_div_fmas_f32 v96, v96, v126, v128
	v_div_fixup_f32 v115, v96, v115, v121
	v_div_scale_f32 v96, s[14:15], v114, v114, v120
	v_rcp_f32_e32 v121, v96
	s_nop 0
	v_fma_f32 v126, -v96, v121, 1.0
	v_fmac_f32_e32 v121, v126, v121
	v_div_scale_f32 v126, vcc, v120, v114, v120
	v_mul_f32_e32 v127, v126, v121
	v_fma_f32 v128, -v96, v127, v126
	v_fmac_f32_e32 v127, v128, v121
	v_fma_f32 v96, -v96, v127, v126
	v_div_fmas_f32 v96, v96, v121, v127
	v_div_fixup_f32 v114, v96, v114, v120
	v_pk_mul_f32 v[120:121], v[116:117], v[114:115]
	v_lshlrev_b64 v[114:115], 11, v[138:139]
	v_lshl_add_u64 v[114:115], s[18:19], 0, v[114:115]
	v_lshl_add_u64 v[114:115], v[114:115], 0, s[12:13]
	v_lshl_add_u64 v[116:117], v[114:115], 0, s[16:17]
	v_lshlrev_b64 v[114:115], 1, v[140:141]
	v_lshl_add_u64 v[126:127], v[116:117], 0, v[114:115]
	v_cvt_pk_bf16_f32 v116, v122, v123
	v_cvt_pk_bf16_f32 v117, v124, v125
	v_cvt_pk_bf16_f32 v119, v120, v121
	v_mul_f32_e32 v96, 0xbfb8aa3b, v110
	global_store_dwordx4 v[126:127], v[116:119], off sc1
	v_mov_b32_e32 v140, v153
	s_nop 0
	v_exp_f32_e32 v116, v96
	v_mul_f32_e32 v96, 0xbfb8aa3b, v111
	v_exp_f32_e32 v117, v96
	s_nop 0
	v_pk_add_f32 v[116:117], v[116:117], 1.0 op_sel_hi:[1,0]
	s_nop 0
	v_div_scale_f32 v96, s[14:15], v117, v117, v111
	v_rcp_f32_e32 v118, v96
	s_nop 0
	v_fma_f32 v119, -v96, v118, 1.0
	v_fmac_f32_e32 v118, v119, v118
	v_div_scale_f32 v119, vcc, v111, v117, v111
	v_mul_f32_e32 v120, v119, v118
	v_fma_f32 v121, -v96, v120, v119
	v_fmac_f32_e32 v120, v121, v118
	v_fma_f32 v96, -v96, v120, v119
	v_div_fmas_f32 v96, v96, v118, v120
	v_div_fixup_f32 v111, v96, v117, v111
	v_div_scale_f32 v96, s[14:15], v116, v116, v110
	v_rcp_f32_e32 v117, v96
	s_nop 0
	v_fma_f32 v118, -v96, v117, 1.0
	v_fmac_f32_e32 v117, v118, v117
	v_div_scale_f32 v118, vcc, v110, v116, v110
	v_mul_f32_e32 v119, v118, v117
	v_fma_f32 v120, -v96, v119, v118
	v_fmac_f32_e32 v119, v120, v117
	v_fma_f32 v96, -v96, v119, v118
	v_div_fmas_f32 v96, v96, v117, v119
	v_div_fixup_f32 v110, v96, v116, v110
	v_mul_f32_e32 v96, 0xbfb8aa3b, v112
	v_pk_mul_f32 v[106:107], v[106:107], v[110:111]
	v_exp_f32_e32 v110, v96
	v_mul_f32_e32 v96, 0xbfb8aa3b, v113
	v_exp_f32_e32 v111, v96
	s_nop 0
	v_pk_add_f32 v[110:111], v[110:111], 1.0 op_sel_hi:[1,0]
	s_nop 0
	v_div_scale_f32 v96, s[14:15], v111, v111, v113
	v_rcp_f32_e32 v116, v96
	s_nop 0
	v_fma_f32 v117, -v96, v116, 1.0
	v_fmac_f32_e32 v116, v117, v116
	v_div_scale_f32 v117, vcc, v113, v111, v113
	v_mul_f32_e32 v118, v117, v116
	v_fma_f32 v119, -v96, v118, v117
	v_fmac_f32_e32 v118, v119, v116
	v_fma_f32 v96, -v96, v118, v117
	v_div_fmas_f32 v96, v96, v116, v118
	v_div_fixup_f32 v111, v96, v111, v113
	v_div_scale_f32 v96, s[14:15], v110, v110, v112
	v_rcp_f32_e32 v113, v96
	s_nop 0
	v_fma_f32 v116, -v96, v113, 1.0
	v_fmac_f32_e32 v113, v116, v113
	v_div_scale_f32 v116, vcc, v112, v110, v112
	v_mul_f32_e32 v117, v116, v113
	v_fma_f32 v118, -v96, v117, v116
	v_fmac_f32_e32 v117, v118, v113
	v_fma_f32 v96, -v96, v117, v116
	v_div_fmas_f32 v96, v96, v113, v117
	v_div_fixup_f32 v110, v96, v110, v112
	v_mul_f32_e32 v96, 0xbfb8aa3b, v102
	v_pk_mul_f32 v[108:109], v[108:109], v[110:111]
	v_exp_f32_e32 v110, v96
	v_mul_f32_e32 v96, 0xbfb8aa3b, v103
	v_exp_f32_e32 v111, v96
	s_nop 0
	v_pk_add_f32 v[110:111], v[110:111], 1.0 op_sel_hi:[1,0]
	s_nop 0
	v_div_scale_f32 v96, s[14:15], v111, v111, v103
	v_rcp_f32_e32 v112, v96
	s_nop 0
	v_fma_f32 v113, -v96, v112, 1.0
	v_fmac_f32_e32 v112, v113, v112
	v_div_scale_f32 v113, vcc, v103, v111, v103
	v_mul_f32_e32 v116, v113, v112
	v_fma_f32 v117, -v96, v116, v113
	v_fmac_f32_e32 v116, v117, v112
	v_fma_f32 v96, -v96, v116, v113
	v_div_fmas_f32 v96, v96, v112, v116
	v_div_fixup_f32 v103, v96, v111, v103
	v_div_scale_f32 v96, s[14:15], v110, v110, v102
	v_rcp_f32_e32 v111, v96
	s_nop 0
	v_fma_f32 v112, -v96, v111, 1.0
	v_fmac_f32_e32 v111, v112, v111
	v_div_scale_f32 v112, vcc, v102, v110, v102
	v_mul_f32_e32 v113, v112, v111
	v_fma_f32 v116, -v96, v113, v112
	v_fmac_f32_e32 v113, v116, v111
	v_fma_f32 v96, -v96, v113, v112
	v_div_fmas_f32 v96, v96, v111, v113
	v_div_fixup_f32 v102, v96, v110, v102
	v_mul_f32_e32 v96, 0xbfb8aa3b, v104
	v_pk_mul_f32 v[102:103], v[98:99], v[102:103]
	v_exp_f32_e32 v98, v96
	v_mul_f32_e32 v96, 0xbfb8aa3b, v105
	v_exp_f32_e32 v99, v96
	s_nop 0
	v_pk_add_f32 v[98:99], v[98:99], 1.0 op_sel_hi:[1,0]
	s_nop 0
	v_div_scale_f32 v96, s[14:15], v99, v99, v105
	v_rcp_f32_e32 v110, v96
	s_nop 0
	v_fma_f32 v111, -v96, v110, 1.0
	v_fmac_f32_e32 v110, v111, v110
	v_div_scale_f32 v111, vcc, v105, v99, v105
	v_mul_f32_e32 v112, v111, v110
	v_fma_f32 v113, -v96, v112, v111
	v_fmac_f32_e32 v112, v113, v110
	v_fma_f32 v96, -v96, v112, v111
	v_div_fmas_f32 v96, v96, v110, v112
	v_div_fixup_f32 v99, v96, v99, v105
	v_div_scale_f32 v96, s[14:15], v98, v98, v104
	v_rcp_f32_e32 v105, v96
	s_nop 0
	v_fma_f32 v110, -v96, v105, 1.0
	v_fmac_f32_e32 v105, v110, v105
	v_div_scale_f32 v110, vcc, v104, v98, v104
	v_mul_f32_e32 v111, v110, v105
	v_fma_f32 v112, -v96, v111, v110
	v_fmac_f32_e32 v111, v112, v105
	v_fma_f32 v96, -v96, v111, v110
	v_div_fmas_f32 v96, v96, v105, v111
	v_div_fixup_f32 v98, v96, v98, v104
	v_pk_mul_f32 v[104:105], v[100:101], v[98:99]
	v_add_u32_e32 v98, 16, v138
	v_ashrrev_i32_e32 v99, 31, v98
	v_lshlrev_b64 v[98:99], 11, v[98:99]
	v_lshl_add_u64 v[98:99], s[18:19], 0, v[98:99]
	v_lshl_add_u64 v[98:99], v[98:99], 0, s[12:13]
	v_lshl_add_u64 v[98:99], v[98:99], 0, s[16:17]
	v_lshl_add_u64 v[110:111], v[98:99], 0, v[114:115]
	v_cvt_pk_bf16_f32 v98, v106, v107
	v_cvt_pk_bf16_f32 v99, v108, v109
	v_cvt_pk_bf16_f32 v100, v102, v103
	v_cvt_pk_bf16_f32 v101, v104, v105
	v_mul_f32_e32 v96, 0xbfb8aa3b, v92
	global_store_dwordx4 v[110:111], v[98:101], off sc1
	s_nop 1
	v_exp_f32_e32 v98, v96
	v_mul_f32_e32 v96, 0xbfb8aa3b, v93
	v_exp_f32_e32 v99, v96
	s_nop 0
	v_pk_add_f32 v[98:99], v[98:99], 1.0 op_sel_hi:[1,0]
	s_nop 0
	v_div_scale_f32 v96, s[14:15], v99, v99, v93
	v_rcp_f32_e32 v100, v96
	s_nop 0
	v_fma_f32 v101, -v96, v100, 1.0
	v_fmac_f32_e32 v100, v101, v100
	v_div_scale_f32 v101, vcc, v93, v99, v93
	v_mul_f32_e32 v102, v101, v100
	v_fma_f32 v103, -v96, v102, v101
	v_fmac_f32_e32 v102, v103, v100
	v_fma_f32 v96, -v96, v102, v101
	v_div_fmas_f32 v96, v96, v100, v102
	v_div_fixup_f32 v93, v96, v99, v93
	v_div_scale_f32 v96, s[14:15], v98, v98, v92
	v_rcp_f32_e32 v99, v96
	s_nop 0
	v_fma_f32 v100, -v96, v99, 1.0
	v_fmac_f32_e32 v99, v100, v99
	v_div_scale_f32 v100, vcc, v92, v98, v92
	v_mul_f32_e32 v101, v100, v99
	v_fma_f32 v102, -v96, v101, v100
	v_fmac_f32_e32 v101, v102, v99
	v_fma_f32 v96, -v96, v101, v100
	v_div_fmas_f32 v96, v96, v99, v101
	v_div_fixup_f32 v92, v96, v98, v92
	v_pk_mul_f32 v[88:89], v[88:89], v[92:93]
	v_mul_f32_e32 v92, 0xbfb8aa3b, v94
	v_mul_f32_e32 v93, 0xbfb8aa3b, v95
	v_exp_f32_e32 v92, v92
	v_exp_f32_e32 v93, v93
	s_nop 0
	v_pk_add_f32 v[92:93], v[92:93], 1.0 op_sel_hi:[1,0]
	s_nop 0
	v_div_scale_f32 v96, s[14:15], v93, v93, v95
	v_rcp_f32_e32 v98, v96
	s_nop 0
	v_fma_f32 v99, -v96, v98, 1.0
	v_fmac_f32_e32 v98, v99, v98
	v_div_scale_f32 v99, vcc, v95, v93, v95
	v_mul_f32_e32 v100, v99, v98
	v_fma_f32 v101, -v96, v100, v99
	v_fmac_f32_e32 v100, v101, v98
	v_fma_f32 v96, -v96, v100, v99
	v_div_fmas_f32 v96, v96, v98, v100
	v_div_fixup_f32 v93, v96, v93, v95
	v_div_scale_f32 v95, s[14:15], v92, v92, v94
	v_rcp_f32_e32 v96, v95
	s_nop 0
	v_fma_f32 v98, -v95, v96, 1.0
	v_fmac_f32_e32 v96, v98, v96
	v_div_scale_f32 v98, vcc, v94, v92, v94
	v_mul_f32_e32 v99, v98, v96
	v_fma_f32 v100, -v95, v99, v98
	v_fmac_f32_e32 v99, v100, v96
	v_fma_f32 v95, -v95, v99, v98
	v_div_fmas_f32 v95, v95, v96, v99
	v_div_fixup_f32 v92, v95, v92, v94
	v_pk_mul_f32 v[90:91], v[90:91], v[92:93]
	v_mul_f32_e32 v92, 0xbfb8aa3b, v84
	v_mul_f32_e32 v93, 0xbfb8aa3b, v85
	v_exp_f32_e32 v92, v92
	v_exp_f32_e32 v93, v93
	s_nop 0
	v_pk_add_f32 v[92:93], v[92:93], 1.0 op_sel_hi:[1,0]
	s_nop 0
	v_div_scale_f32 v94, s[14:15], v93, v93, v85
	v_rcp_f32_e32 v95, v94
	s_nop 0
	v_fma_f32 v96, -v94, v95, 1.0
	v_fmac_f32_e32 v95, v96, v95
	v_div_scale_f32 v96, vcc, v85, v93, v85
	v_mul_f32_e32 v98, v96, v95
	v_fma_f32 v99, -v94, v98, v96
	v_fmac_f32_e32 v98, v99, v95
	v_fma_f32 v94, -v94, v98, v96
	v_div_fmas_f32 v94, v94, v95, v98
	v_div_fixup_f32 v85, v94, v93, v85
	v_div_scale_f32 v93, s[14:15], v92, v92, v84
	v_rcp_f32_e32 v94, v93
	s_nop 0
	v_fma_f32 v95, -v93, v94, 1.0
	v_fmac_f32_e32 v94, v95, v94
	v_div_scale_f32 v95, vcc, v84, v92, v84
	v_mul_f32_e32 v96, v95, v94
	v_fma_f32 v98, -v93, v96, v95
	v_fmac_f32_e32 v96, v98, v94
	v_fma_f32 v93, -v93, v96, v95
	v_div_fmas_f32 v93, v93, v94, v96
	v_div_fixup_f32 v84, v93, v92, v84
	v_pk_mul_f32 v[84:85], v[80:81], v[84:85]
	v_mul_f32_e32 v80, 0xbfb8aa3b, v86
	v_mul_f32_e32 v81, 0xbfb8aa3b, v87
	v_exp_f32_e32 v80, v80
	v_exp_f32_e32 v81, v81
	s_nop 0
	v_pk_add_f32 v[80:81], v[80:81], 1.0 op_sel_hi:[1,0]
	s_nop 0
	v_div_scale_f32 v92, s[14:15], v81, v81, v87
	v_rcp_f32_e32 v93, v92
	s_nop 0
	v_fma_f32 v94, -v92, v93, 1.0
	v_fmac_f32_e32 v93, v94, v93
	v_div_scale_f32 v94, vcc, v87, v81, v87
	v_mul_f32_e32 v95, v94, v93
	v_fma_f32 v96, -v92, v95, v94
	v_fmac_f32_e32 v95, v96, v93
	v_fma_f32 v92, -v92, v95, v94
	v_div_fmas_f32 v92, v92, v93, v95
	v_div_fixup_f32 v81, v92, v81, v87
	v_div_scale_f32 v87, s[14:15], v80, v80, v86
	v_rcp_f32_e32 v92, v87
	s_nop 0
	v_fma_f32 v93, -v87, v92, 1.0
	v_fmac_f32_e32 v92, v93, v92
	v_div_scale_f32 v93, vcc, v86, v80, v86
	v_mul_f32_e32 v94, v93, v92
	v_fma_f32 v95, -v87, v94, v93
	v_fmac_f32_e32 v94, v95, v92
	v_fma_f32 v87, -v87, v94, v93
	v_div_fmas_f32 v87, v87, v92, v94
	v_div_fixup_f32 v80, v87, v80, v86
	v_pk_mul_f32 v[86:87], v[82:83], v[80:81]
	v_add_u32_e32 v80, 32, v138
	v_ashrrev_i32_e32 v81, 31, v80
	v_lshlrev_b64 v[80:81], 11, v[80:81]
	v_lshl_add_u64 v[80:81], s[18:19], 0, v[80:81]
	v_lshl_add_u64 v[80:81], v[80:81], 0, s[12:13]
	v_lshl_add_u64 v[80:81], v[80:81], 0, s[16:17]
	v_lshl_add_u64 v[92:93], v[80:81], 0, v[114:115]
	v_cvt_pk_bf16_f32 v80, v88, v89
	v_cvt_pk_bf16_f32 v81, v90, v91
	v_cvt_pk_bf16_f32 v82, v84, v85
	v_cvt_pk_bf16_f32 v83, v86, v87
	global_store_dwordx4 v[92:93], v[80:83], off sc1
	s_nop 1
	v_mul_f32_e32 v80, 0xbfb8aa3b, v76
	v_mul_f32_e32 v81, 0xbfb8aa3b, v77
	v_exp_f32_e32 v80, v80
	v_exp_f32_e32 v81, v81
	s_nop 0
	v_pk_add_f32 v[80:81], v[80:81], 1.0 op_sel_hi:[1,0]
	s_nop 0
	v_div_scale_f32 v82, s[14:15], v81, v81, v77
	v_rcp_f32_e32 v83, v82
	s_nop 0
	v_fma_f32 v84, -v82, v83, 1.0
	v_fmac_f32_e32 v83, v84, v83
	v_div_scale_f32 v84, vcc, v77, v81, v77
	v_mul_f32_e32 v85, v84, v83
	v_fma_f32 v86, -v82, v85, v84
	v_fmac_f32_e32 v85, v86, v83
	v_fma_f32 v82, -v82, v85, v84
	v_div_fmas_f32 v82, v82, v83, v85
	v_div_fixup_f32 v77, v82, v81, v77
	v_div_scale_f32 v81, s[14:15], v80, v80, v76
	v_rcp_f32_e32 v82, v81
	s_nop 0
	v_fma_f32 v83, -v81, v82, 1.0
	v_fmac_f32_e32 v82, v83, v82
	v_div_scale_f32 v83, vcc, v76, v80, v76
	v_mul_f32_e32 v84, v83, v82
	v_fma_f32 v85, -v81, v84, v83
	v_fmac_f32_e32 v84, v85, v82
	v_fma_f32 v81, -v81, v84, v83
	v_div_fmas_f32 v81, v81, v82, v84
	v_div_fixup_f32 v76, v81, v80, v76
	v_pk_mul_f32 v[72:73], v[72:73], v[76:77]
	v_mul_f32_e32 v76, 0xbfb8aa3b, v78
	v_mul_f32_e32 v77, 0xbfb8aa3b, v79
	v_exp_f32_e32 v76, v76
	v_exp_f32_e32 v77, v77
	s_nop 0
	v_pk_add_f32 v[76:77], v[76:77], 1.0 op_sel_hi:[1,0]
	s_nop 0
	v_div_scale_f32 v80, s[14:15], v77, v77, v79
	v_rcp_f32_e32 v81, v80
	s_nop 0
	v_fma_f32 v82, -v80, v81, 1.0
	v_fmac_f32_e32 v81, v82, v81
	v_div_scale_f32 v82, vcc, v79, v77, v79
	v_mul_f32_e32 v83, v82, v81
	v_fma_f32 v84, -v80, v83, v82
	v_fmac_f32_e32 v83, v84, v81
	v_fma_f32 v80, -v80, v83, v82
	v_div_fmas_f32 v80, v80, v81, v83
	v_div_fixup_f32 v77, v80, v77, v79
	v_div_scale_f32 v79, s[14:15], v76, v76, v78
	v_rcp_f32_e32 v80, v79
	s_nop 0
	v_fma_f32 v81, -v79, v80, 1.0
	v_fmac_f32_e32 v80, v81, v80
	v_div_scale_f32 v81, vcc, v78, v76, v78
	v_mul_f32_e32 v82, v81, v80
	v_fma_f32 v83, -v79, v82, v81
	v_fmac_f32_e32 v82, v83, v80
	v_fma_f32 v79, -v79, v82, v81
	v_div_fmas_f32 v79, v79, v80, v82
	v_div_fixup_f32 v76, v79, v76, v78
	v_pk_mul_f32 v[74:75], v[74:75], v[76:77]
	v_mul_f32_e32 v76, 0xbfb8aa3b, v68
	v_mul_f32_e32 v77, 0xbfb8aa3b, v69
	v_exp_f32_e32 v76, v76
	v_exp_f32_e32 v77, v77
	s_nop 0
	v_pk_add_f32 v[76:77], v[76:77], 1.0 op_sel_hi:[1,0]
	s_nop 0
	v_div_scale_f32 v78, s[14:15], v77, v77, v69
	v_rcp_f32_e32 v79, v78
	s_nop 0
	v_fma_f32 v80, -v78, v79, 1.0
	v_fmac_f32_e32 v79, v80, v79
	v_div_scale_f32 v80, vcc, v69, v77, v69
	v_mul_f32_e32 v81, v80, v79
	v_fma_f32 v82, -v78, v81, v80
	v_fmac_f32_e32 v81, v82, v79
	v_fma_f32 v78, -v78, v81, v80
	v_div_fmas_f32 v78, v78, v79, v81
	v_div_fixup_f32 v69, v78, v77, v69
	v_div_scale_f32 v77, s[14:15], v76, v76, v68
	v_rcp_f32_e32 v78, v77
	s_nop 0
	v_fma_f32 v79, -v77, v78, 1.0
	v_fmac_f32_e32 v78, v79, v78
	v_div_scale_f32 v79, vcc, v68, v76, v68
	v_mul_f32_e32 v80, v79, v78
	v_fma_f32 v81, -v77, v80, v79
	v_fmac_f32_e32 v80, v81, v78
	v_fma_f32 v77, -v77, v80, v79
	v_div_fmas_f32 v77, v77, v78, v80
	v_div_fixup_f32 v68, v77, v76, v68
	v_pk_mul_f32 v[68:69], v[64:65], v[68:69]
	v_mul_f32_e32 v64, 0xbfb8aa3b, v70
	v_mul_f32_e32 v65, 0xbfb8aa3b, v71
	v_exp_f32_e32 v64, v64
	v_exp_f32_e32 v65, v65
	s_nop 0
	v_pk_add_f32 v[64:65], v[64:65], 1.0 op_sel_hi:[1,0]
	s_nop 0
	v_div_scale_f32 v76, s[14:15], v65, v65, v71
	v_rcp_f32_e32 v77, v76
	s_nop 0
	v_fma_f32 v78, -v76, v77, 1.0
	v_fmac_f32_e32 v77, v78, v77
	v_div_scale_f32 v78, vcc, v71, v65, v71
	v_mul_f32_e32 v79, v78, v77
	v_fma_f32 v80, -v76, v79, v78
	v_fmac_f32_e32 v79, v80, v77
	v_fma_f32 v76, -v76, v79, v78
	v_div_fmas_f32 v76, v76, v77, v79
	v_div_fixup_f32 v65, v76, v65, v71
	v_div_scale_f32 v71, s[14:15], v64, v64, v70
	v_rcp_f32_e32 v76, v71
	s_nop 0
	v_fma_f32 v77, -v71, v76, 1.0
	v_fmac_f32_e32 v76, v77, v76
	v_div_scale_f32 v77, vcc, v70, v64, v70
	v_mul_f32_e32 v78, v77, v76
	v_fma_f32 v79, -v71, v78, v77
	v_fmac_f32_e32 v78, v79, v76
	v_fma_f32 v71, -v71, v78, v77
	v_div_fmas_f32 v71, v71, v76, v78
	v_div_fixup_f32 v64, v71, v64, v70
	v_pk_mul_f32 v[70:71], v[66:67], v[64:65]
	v_add_u32_e32 v64, 48, v138
	v_ashrrev_i32_e32 v65, 31, v64
	v_lshlrev_b64 v[64:65], 11, v[64:65]
	v_lshl_add_u64 v[64:65], s[18:19], 0, v[64:65]
	v_lshl_add_u64 v[64:65], v[64:65], 0, s[12:13]
	v_lshl_add_u64 v[64:65], v[64:65], 0, s[16:17]
	v_lshl_add_u64 v[76:77], v[64:65], 0, v[114:115]
	v_cvt_pk_bf16_f32 v64, v72, v73
	v_cvt_pk_bf16_f32 v65, v74, v75
	v_cvt_pk_bf16_f32 v66, v68, v69
	v_cvt_pk_bf16_f32 v67, v70, v71
	global_store_dwordx4 v[76:77], v[64:67], off sc1
	s_nop 1
	v_mul_f32_e32 v65, 0xbfb8aa3b, v60
	v_exp_f32_e32 v66, v65
	v_mul_f32_e32 v65, 0xbfb8aa3b, v61
	v_exp_f32_e32 v67, v65
	v_add_u32_e32 v64, 0x80, v138
	v_pk_add_f32 v[66:67], v[66:67], 1.0 op_sel_hi:[1,0]
	s_nop 0
	v_div_scale_f32 v65, s[14:15], v67, v67, v61
	v_rcp_f32_e32 v68, v65
	s_nop 0
	v_fma_f32 v69, -v65, v68, 1.0
	v_fmac_f32_e32 v68, v69, v68
	v_div_scale_f32 v69, vcc, v61, v67, v61
	v_mul_f32_e32 v70, v69, v68
	v_fma_f32 v71, -v65, v70, v69
	v_fmac_f32_e32 v70, v71, v68
	v_fma_f32 v65, -v65, v70, v69
	v_div_fmas_f32 v65, v65, v68, v70
	v_div_fixup_f32 v61, v65, v67, v61
	v_div_scale_f32 v65, s[14:15], v66, v66, v60
	v_rcp_f32_e32 v67, v65
	s_nop 0
	v_fma_f32 v68, -v65, v67, 1.0
	v_fmac_f32_e32 v67, v68, v67
	v_div_scale_f32 v68, vcc, v60, v66, v60
	v_mul_f32_e32 v69, v68, v67
	v_fma_f32 v70, -v65, v69, v68
	v_fmac_f32_e32 v69, v70, v67
	v_fma_f32 v65, -v65, v69, v68
	v_div_fmas_f32 v65, v65, v67, v69
	v_div_fixup_f32 v60, v65, v66, v60
	v_pk_mul_f32 v[56:57], v[56:57], v[60:61]
	v_mul_f32_e32 v60, 0xbfb8aa3b, v62
	v_mul_f32_e32 v61, 0xbfb8aa3b, v63
	v_exp_f32_e32 v60, v60
	v_exp_f32_e32 v61, v61
	s_nop 0
	v_pk_add_f32 v[60:61], v[60:61], 1.0 op_sel_hi:[1,0]
	s_nop 0
	v_div_scale_f32 v65, s[14:15], v61, v61, v63
	v_rcp_f32_e32 v66, v65
	s_nop 0
	v_fma_f32 v67, -v65, v66, 1.0
	v_fmac_f32_e32 v66, v67, v66
	v_div_scale_f32 v67, vcc, v63, v61, v63
	v_mul_f32_e32 v68, v67, v66
	v_fma_f32 v69, -v65, v68, v67
	v_fmac_f32_e32 v68, v69, v66
	v_fma_f32 v65, -v65, v68, v67
	v_div_fmas_f32 v65, v65, v66, v68
	v_div_fixup_f32 v61, v65, v61, v63
	v_div_scale_f32 v63, s[14:15], v60, v60, v62
	v_rcp_f32_e32 v65, v63
	s_nop 0
	v_fma_f32 v66, -v63, v65, 1.0
	v_fmac_f32_e32 v65, v66, v65
	v_div_scale_f32 v66, vcc, v62, v60, v62
	v_mul_f32_e32 v67, v66, v65
	v_fma_f32 v68, -v63, v67, v66
	v_fmac_f32_e32 v67, v68, v65
	v_fma_f32 v63, -v63, v67, v66
	v_div_fmas_f32 v63, v63, v65, v67
	v_div_fixup_f32 v60, v63, v60, v62
	v_pk_mul_f32 v[58:59], v[58:59], v[60:61]
	v_mul_f32_e32 v60, 0xbfb8aa3b, v52
	v_mul_f32_e32 v61, 0xbfb8aa3b, v53
	v_exp_f32_e32 v60, v60
	v_exp_f32_e32 v61, v61
	s_nop 0
	v_pk_add_f32 v[60:61], v[60:61], 1.0 op_sel_hi:[1,0]
	s_nop 0
	v_div_scale_f32 v62, s[14:15], v61, v61, v53
	v_rcp_f32_e32 v63, v62
	s_nop 0
	v_fma_f32 v65, -v62, v63, 1.0
	v_fmac_f32_e32 v63, v65, v63
	v_div_scale_f32 v65, vcc, v53, v61, v53
	v_mul_f32_e32 v66, v65, v63
	v_fma_f32 v67, -v62, v66, v65
	v_fmac_f32_e32 v66, v67, v63
	v_fma_f32 v62, -v62, v66, v65
	v_div_fmas_f32 v62, v62, v63, v66
	v_div_fixup_f32 v53, v62, v61, v53
	v_div_scale_f32 v61, s[14:15], v60, v60, v52
	v_rcp_f32_e32 v62, v61
	s_nop 0
	v_fma_f32 v63, -v61, v62, 1.0
	v_fmac_f32_e32 v62, v63, v62
	v_div_scale_f32 v63, vcc, v52, v60, v52
	v_mul_f32_e32 v65, v63, v62
	v_fma_f32 v66, -v61, v65, v63
	v_fmac_f32_e32 v65, v66, v62
	v_fma_f32 v61, -v61, v65, v63
	v_div_fmas_f32 v61, v61, v62, v65
	v_div_fixup_f32 v52, v61, v60, v52
	v_pk_mul_f32 v[52:53], v[48:49], v[52:53]
	v_mul_f32_e32 v48, 0xbfb8aa3b, v54
	v_mul_f32_e32 v49, 0xbfb8aa3b, v55
	v_exp_f32_e32 v48, v48
	v_exp_f32_e32 v49, v49
	s_nop 0
	v_pk_add_f32 v[48:49], v[48:49], 1.0 op_sel_hi:[1,0]
	s_nop 0
	v_div_scale_f32 v60, s[14:15], v49, v49, v55
	v_rcp_f32_e32 v61, v60
	s_nop 0
	v_fma_f32 v62, -v60, v61, 1.0
	v_fmac_f32_e32 v61, v62, v61
	v_div_scale_f32 v62, vcc, v55, v49, v55
	v_mul_f32_e32 v63, v62, v61
	v_fma_f32 v65, -v60, v63, v62
	v_fmac_f32_e32 v63, v65, v61
	v_fma_f32 v60, -v60, v63, v62
	v_div_fmas_f32 v60, v60, v61, v63
	v_div_fixup_f32 v49, v60, v49, v55
	v_div_scale_f32 v55, s[14:15], v48, v48, v54
	v_rcp_f32_e32 v60, v55
	v_ashrrev_i32_e32 v65, 31, v64
	v_fma_f32 v61, -v55, v60, 1.0
	v_fmac_f32_e32 v60, v61, v60
	v_div_scale_f32 v61, vcc, v54, v48, v54
	v_mul_f32_e32 v62, v61, v60
	v_fma_f32 v63, -v55, v62, v61
	v_fmac_f32_e32 v62, v63, v60
	v_fma_f32 v55, -v55, v62, v61
	v_div_fmas_f32 v55, v55, v60, v62
	v_div_fixup_f32 v48, v55, v48, v54
	v_pk_mul_f32 v[54:55], v[50:51], v[48:49]
	v_lshlrev_b64 v[48:49], 11, v[64:65]
	v_lshl_add_u64 v[48:49], s[18:19], 0, v[48:49]
	v_lshl_add_u64 v[48:49], v[48:49], 0, s[12:13]
	v_lshl_add_u64 v[48:49], v[48:49], 0, s[16:17]
	v_lshl_add_u64 v[60:61], v[48:49], 0, v[114:115]
	v_cvt_pk_bf16_f32 v48, v56, v57
	v_cvt_pk_bf16_f32 v49, v58, v59
	v_cvt_pk_bf16_f32 v50, v52, v53
	v_cvt_pk_bf16_f32 v51, v54, v55
	global_store_dwordx4 v[60:61], v[48:51], off sc1
	s_nop 1
	v_mul_f32_e32 v48, 0xbfb8aa3b, v44
	v_mul_f32_e32 v49, 0xbfb8aa3b, v45
	v_exp_f32_e32 v48, v48
	v_exp_f32_e32 v49, v49
	s_nop 0
	v_pk_add_f32 v[48:49], v[48:49], 1.0 op_sel_hi:[1,0]
	s_nop 0
	v_div_scale_f32 v50, s[14:15], v49, v49, v45
	v_rcp_f32_e32 v51, v50
	s_nop 0
	v_fma_f32 v52, -v50, v51, 1.0
	v_fmac_f32_e32 v51, v52, v51
	v_div_scale_f32 v52, vcc, v45, v49, v45
	v_mul_f32_e32 v53, v52, v51
	v_fma_f32 v54, -v50, v53, v52
	v_fmac_f32_e32 v53, v54, v51
	v_fma_f32 v50, -v50, v53, v52
	v_div_fmas_f32 v50, v50, v51, v53
	v_div_fixup_f32 v45, v50, v49, v45
	v_div_scale_f32 v49, s[14:15], v48, v48, v44
	v_rcp_f32_e32 v50, v49
	s_nop 0
	v_fma_f32 v51, -v49, v50, 1.0
	v_fmac_f32_e32 v50, v51, v50
	v_div_scale_f32 v51, vcc, v44, v48, v44
	v_mul_f32_e32 v52, v51, v50
	v_fma_f32 v53, -v49, v52, v51
	v_fmac_f32_e32 v52, v53, v50
	v_fma_f32 v49, -v49, v52, v51
	v_div_fmas_f32 v49, v49, v50, v52
	v_div_fixup_f32 v44, v49, v48, v44
	v_pk_mul_f32 v[40:41], v[44:45], v[40:41]
	v_mul_f32_e32 v44, 0xbfb8aa3b, v46
	v_mul_f32_e32 v45, 0xbfb8aa3b, v47
	v_exp_f32_e32 v44, v44
	v_exp_f32_e32 v45, v45
	s_nop 0
	v_pk_add_f32 v[44:45], v[44:45], 1.0 op_sel_hi:[1,0]
	s_nop 0
	v_div_scale_f32 v48, s[14:15], v45, v45, v47
	v_rcp_f32_e32 v49, v48
	s_nop 0
	v_fma_f32 v50, -v48, v49, 1.0
	v_fmac_f32_e32 v49, v50, v49
	v_div_scale_f32 v50, vcc, v47, v45, v47
	v_mul_f32_e32 v51, v50, v49
	v_fma_f32 v52, -v48, v51, v50
	v_fmac_f32_e32 v51, v52, v49
	v_fma_f32 v48, -v48, v51, v50
	v_div_fmas_f32 v48, v48, v49, v51
	v_div_fixup_f32 v45, v48, v45, v47
	v_div_scale_f32 v47, s[14:15], v44, v44, v46
	v_rcp_f32_e32 v48, v47
	s_nop 0
	v_fma_f32 v49, -v47, v48, 1.0
	v_fmac_f32_e32 v48, v49, v48
	v_div_scale_f32 v49, vcc, v46, v44, v46
	v_mul_f32_e32 v50, v49, v48
	v_fma_f32 v51, -v47, v50, v49
	v_fmac_f32_e32 v50, v51, v48
	v_fma_f32 v47, -v47, v50, v49
	v_div_fmas_f32 v47, v47, v48, v50
	v_div_fixup_f32 v44, v47, v44, v46
	v_pk_mul_f32 v[42:43], v[44:45], v[42:43]
	v_mul_f32_e32 v44, 0xbfb8aa3b, v36
	v_mul_f32_e32 v45, 0xbfb8aa3b, v37
	v_exp_f32_e32 v44, v44
	v_exp_f32_e32 v45, v45
	s_nop 0
	v_pk_add_f32 v[44:45], v[44:45], 1.0 op_sel_hi:[1,0]
	s_nop 0
	v_div_scale_f32 v46, s[14:15], v45, v45, v37
	v_rcp_f32_e32 v47, v46
	s_nop 0
	v_fma_f32 v48, -v46, v47, 1.0
	v_fmac_f32_e32 v47, v48, v47
	v_div_scale_f32 v48, vcc, v37, v45, v37
	v_mul_f32_e32 v49, v48, v47
	v_fma_f32 v50, -v46, v49, v48
	v_fmac_f32_e32 v49, v50, v47
	v_fma_f32 v46, -v46, v49, v48
	v_div_fmas_f32 v46, v46, v47, v49
	v_div_fixup_f32 v37, v46, v45, v37
	v_div_scale_f32 v45, s[14:15], v44, v44, v36
	v_rcp_f32_e32 v46, v45
	s_nop 0
	v_fma_f32 v47, -v45, v46, 1.0
	v_fmac_f32_e32 v46, v47, v46
	v_div_scale_f32 v47, vcc, v36, v44, v36
	v_mul_f32_e32 v48, v47, v46
	v_fma_f32 v49, -v45, v48, v47
	v_fmac_f32_e32 v48, v49, v46
	v_fma_f32 v45, -v45, v48, v47
	v_div_fmas_f32 v45, v45, v46, v48
	v_div_fixup_f32 v36, v45, v44, v36
	v_pk_mul_f32 v[36:37], v[36:37], v[32:33]
	v_mul_f32_e32 v32, 0xbfb8aa3b, v38
	v_mul_f32_e32 v33, 0xbfb8aa3b, v39
	v_exp_f32_e32 v32, v32
	v_exp_f32_e32 v33, v33
	s_nop 0
	v_pk_add_f32 v[32:33], v[32:33], 1.0 op_sel_hi:[1,0]
	s_nop 0
	v_div_scale_f32 v44, s[14:15], v33, v33, v39
	v_rcp_f32_e32 v45, v44
	s_nop 0
	v_fma_f32 v46, -v44, v45, 1.0
	v_fmac_f32_e32 v45, v46, v45
	v_div_scale_f32 v46, vcc, v39, v33, v39
	v_mul_f32_e32 v47, v46, v45
	v_fma_f32 v48, -v44, v47, v46
	v_fmac_f32_e32 v47, v48, v45
	v_fma_f32 v44, -v44, v47, v46
	v_div_fmas_f32 v44, v44, v45, v47
	v_div_fixup_f32 v33, v44, v33, v39
	v_div_scale_f32 v39, s[14:15], v32, v32, v38
	v_rcp_f32_e32 v44, v39
	s_nop 0
	v_fma_f32 v45, -v39, v44, 1.0
	v_fmac_f32_e32 v44, v45, v44
	v_div_scale_f32 v45, vcc, v38, v32, v38
	v_mul_f32_e32 v46, v45, v44
	v_fma_f32 v47, -v39, v46, v45
	v_fmac_f32_e32 v46, v47, v44
	v_fma_f32 v39, -v39, v46, v45
	v_div_fmas_f32 v39, v39, v44, v46
	v_div_fixup_f32 v32, v39, v32, v38
	v_pk_mul_f32 v[38:39], v[32:33], v[34:35]
	v_add_u32_e32 v32, 0x90, v138
	v_ashrrev_i32_e32 v33, 31, v32
	v_lshlrev_b64 v[32:33], 11, v[32:33]
	v_lshl_add_u64 v[32:33], s[18:19], 0, v[32:33]
	v_lshl_add_u64 v[32:33], v[32:33], 0, s[12:13]
	v_lshl_add_u64 v[32:33], v[32:33], 0, s[16:17]
	v_lshl_add_u64 v[44:45], v[32:33], 0, v[114:115]
	v_cvt_pk_bf16_f32 v32, v40, v41
	v_cvt_pk_bf16_f32 v33, v42, v43
	v_cvt_pk_bf16_f32 v34, v36, v37
	v_cvt_pk_bf16_f32 v35, v38, v39
	global_store_dwordx4 v[44:45], v[32:35], off sc1
	s_nop 1
	v_mul_f32_e32 v32, 0xbfb8aa3b, v28
	v_mul_f32_e32 v33, 0xbfb8aa3b, v29
	v_exp_f32_e32 v32, v32
	v_exp_f32_e32 v33, v33
	s_nop 0
	v_pk_add_f32 v[32:33], v[32:33], 1.0 op_sel_hi:[1,0]
	s_nop 0
	v_div_scale_f32 v34, s[14:15], v33, v33, v29
	v_rcp_f32_e32 v35, v34
	s_nop 0
	v_fma_f32 v36, -v34, v35, 1.0
	v_fmac_f32_e32 v35, v36, v35
	v_div_scale_f32 v36, vcc, v29, v33, v29
	v_mul_f32_e32 v37, v36, v35
	v_fma_f32 v38, -v34, v37, v36
	v_fmac_f32_e32 v37, v38, v35
	v_fma_f32 v34, -v34, v37, v36
	v_div_fmas_f32 v34, v34, v35, v37
	v_div_fixup_f32 v29, v34, v33, v29
	v_div_scale_f32 v33, s[14:15], v32, v32, v28
	v_rcp_f32_e32 v34, v33
	s_nop 0
	v_fma_f32 v35, -v33, v34, 1.0
	v_fmac_f32_e32 v34, v35, v34
	v_div_scale_f32 v35, vcc, v28, v32, v28
	v_mul_f32_e32 v36, v35, v34
	v_fma_f32 v37, -v33, v36, v35
	v_fmac_f32_e32 v36, v37, v34
	v_fma_f32 v33, -v33, v36, v35
	v_div_fmas_f32 v33, v33, v34, v36
	v_div_fixup_f32 v28, v33, v32, v28
	v_pk_mul_f32 v[24:25], v[28:29], v[24:25]
	v_mul_f32_e32 v28, 0xbfb8aa3b, v30
	v_mul_f32_e32 v29, 0xbfb8aa3b, v31
	v_exp_f32_e32 v28, v28
	v_exp_f32_e32 v29, v29
	s_nop 0
	v_pk_add_f32 v[28:29], v[28:29], 1.0 op_sel_hi:[1,0]
	s_nop 0
	v_div_scale_f32 v32, s[14:15], v29, v29, v31
	v_rcp_f32_e32 v33, v32
	s_nop 0
	v_fma_f32 v34, -v32, v33, 1.0
	v_fmac_f32_e32 v33, v34, v33
	v_div_scale_f32 v34, vcc, v31, v29, v31
	v_mul_f32_e32 v35, v34, v33
	v_fma_f32 v36, -v32, v35, v34
	v_fmac_f32_e32 v35, v36, v33
	v_fma_f32 v32, -v32, v35, v34
	v_div_fmas_f32 v32, v32, v33, v35
	v_div_fixup_f32 v29, v32, v29, v31
	v_div_scale_f32 v31, s[14:15], v28, v28, v30
	v_rcp_f32_e32 v32, v31
	s_nop 0
	v_fma_f32 v33, -v31, v32, 1.0
	v_fmac_f32_e32 v32, v33, v32
	v_div_scale_f32 v33, vcc, v30, v28, v30
	v_mul_f32_e32 v34, v33, v32
	v_fma_f32 v35, -v31, v34, v33
	v_fmac_f32_e32 v34, v35, v32
	v_fma_f32 v31, -v31, v34, v33
	v_div_fmas_f32 v31, v31, v32, v34
	v_div_fixup_f32 v28, v31, v28, v30
	v_pk_mul_f32 v[26:27], v[28:29], v[26:27]
	v_mul_f32_e32 v28, 0xbfb8aa3b, v20
	v_mul_f32_e32 v29, 0xbfb8aa3b, v21
	v_exp_f32_e32 v28, v28
	v_exp_f32_e32 v29, v29
	s_nop 0
	v_pk_add_f32 v[28:29], v[28:29], 1.0 op_sel_hi:[1,0]
	s_nop 0
	v_div_scale_f32 v30, s[14:15], v29, v29, v21
	v_rcp_f32_e32 v31, v30
	s_nop 0
	v_fma_f32 v32, -v30, v31, 1.0
	v_fmac_f32_e32 v31, v32, v31
	v_div_scale_f32 v32, vcc, v21, v29, v21
	v_mul_f32_e32 v33, v32, v31
	v_fma_f32 v34, -v30, v33, v32
	v_fmac_f32_e32 v33, v34, v31
	v_fma_f32 v30, -v30, v33, v32
	v_div_fmas_f32 v30, v30, v31, v33
	v_div_fixup_f32 v21, v30, v29, v21
	v_div_scale_f32 v29, s[14:15], v28, v28, v20
	v_rcp_f32_e32 v30, v29
	s_nop 0
	v_fma_f32 v31, -v29, v30, 1.0
	v_fmac_f32_e32 v30, v31, v30
	v_div_scale_f32 v31, vcc, v20, v28, v20
	v_mul_f32_e32 v32, v31, v30
	v_fma_f32 v33, -v29, v32, v31
	v_fmac_f32_e32 v32, v33, v30
	v_fma_f32 v29, -v29, v32, v31
	v_div_fmas_f32 v29, v29, v30, v32
	v_div_fixup_f32 v20, v29, v28, v20
	v_pk_mul_f32 v[20:21], v[20:21], v[16:17]
	v_mul_f32_e32 v16, 0xbfb8aa3b, v22
	v_mul_f32_e32 v17, 0xbfb8aa3b, v23
	v_exp_f32_e32 v16, v16
	v_exp_f32_e32 v17, v17
	s_nop 0
	v_pk_add_f32 v[16:17], v[16:17], 1.0 op_sel_hi:[1,0]
	s_nop 0
	v_div_scale_f32 v28, s[14:15], v17, v17, v23
	v_rcp_f32_e32 v29, v28
	s_nop 0
	v_fma_f32 v30, -v28, v29, 1.0
	v_fmac_f32_e32 v29, v30, v29
	v_div_scale_f32 v30, vcc, v23, v17, v23
	v_mul_f32_e32 v31, v30, v29
	v_fma_f32 v32, -v28, v31, v30
	v_fmac_f32_e32 v31, v32, v29
	v_fma_f32 v28, -v28, v31, v30
	v_div_fmas_f32 v28, v28, v29, v31
	v_div_fixup_f32 v17, v28, v17, v23
	v_div_scale_f32 v23, s[14:15], v16, v16, v22
	v_rcp_f32_e32 v28, v23
	s_nop 0
	v_fma_f32 v29, -v23, v28, 1.0
	v_fmac_f32_e32 v28, v29, v28
	v_div_scale_f32 v29, vcc, v22, v16, v22
	v_mul_f32_e32 v30, v29, v28
	v_fma_f32 v31, -v23, v30, v29
	v_fmac_f32_e32 v30, v31, v28
	v_fma_f32 v23, -v23, v30, v29
	v_div_fmas_f32 v23, v23, v28, v30
	v_div_fixup_f32 v16, v23, v16, v22
	v_pk_mul_f32 v[22:23], v[16:17], v[18:19]
	v_add_u32_e32 v16, 0xa0, v138
	v_ashrrev_i32_e32 v17, 31, v16
	v_lshlrev_b64 v[16:17], 11, v[16:17]
	v_lshl_add_u64 v[16:17], s[18:19], 0, v[16:17]
	v_lshl_add_u64 v[16:17], v[16:17], 0, s[12:13]
	v_lshl_add_u64 v[16:17], v[16:17], 0, s[16:17]
	v_lshl_add_u64 v[28:29], v[16:17], 0, v[114:115]
	v_cvt_pk_bf16_f32 v16, v24, v25
	v_cvt_pk_bf16_f32 v17, v26, v27
	v_cvt_pk_bf16_f32 v18, v20, v21
	v_cvt_pk_bf16_f32 v19, v22, v23
	global_store_dwordx4 v[28:29], v[16:19], off sc1
	s_nop 1
	v_mul_f32_e32 v16, 0xbfb8aa3b, v12
	v_mul_f32_e32 v17, 0xbfb8aa3b, v13
	v_exp_f32_e32 v16, v16
	v_exp_f32_e32 v17, v17
	s_nop 0
	v_pk_add_f32 v[16:17], v[16:17], 1.0 op_sel_hi:[1,0]
	s_nop 0
	v_div_scale_f32 v18, s[14:15], v17, v17, v13
	v_rcp_f32_e32 v19, v18
	s_nop 0
	v_fma_f32 v20, -v18, v19, 1.0
	v_fmac_f32_e32 v19, v20, v19
	v_div_scale_f32 v20, vcc, v13, v17, v13
	v_mul_f32_e32 v21, v20, v19
	v_fma_f32 v22, -v18, v21, v20
	v_fmac_f32_e32 v21, v22, v19
	v_fma_f32 v18, -v18, v21, v20
	v_div_fmas_f32 v18, v18, v19, v21
	v_div_fixup_f32 v13, v18, v17, v13
	v_div_scale_f32 v17, s[14:15], v16, v16, v12
	v_rcp_f32_e32 v18, v17
	s_nop 0
	v_fma_f32 v19, -v17, v18, 1.0
	v_fmac_f32_e32 v18, v19, v18
	v_div_scale_f32 v19, vcc, v12, v16, v12
	v_mul_f32_e32 v20, v19, v18
	v_fma_f32 v21, -v17, v20, v19
	v_fmac_f32_e32 v20, v21, v18
	v_fma_f32 v17, -v17, v20, v19
	v_div_fmas_f32 v17, v17, v18, v20
	v_div_fixup_f32 v12, v17, v16, v12
	v_pk_mul_f32 v[8:9], v[12:13], v[8:9]
	v_mul_f32_e32 v12, 0xbfb8aa3b, v14
	v_mul_f32_e32 v13, 0xbfb8aa3b, v15
	v_exp_f32_e32 v12, v12
	v_exp_f32_e32 v13, v13
	s_nop 0
	v_pk_add_f32 v[12:13], v[12:13], 1.0 op_sel_hi:[1,0]
	s_nop 0
	v_div_scale_f32 v16, s[14:15], v13, v13, v15
	v_rcp_f32_e32 v17, v16
	s_nop 0
	v_fma_f32 v18, -v16, v17, 1.0
	v_fmac_f32_e32 v17, v18, v17
	v_div_scale_f32 v18, vcc, v15, v13, v15
	v_mul_f32_e32 v19, v18, v17
	v_fma_f32 v20, -v16, v19, v18
	v_fmac_f32_e32 v19, v20, v17
	v_fma_f32 v16, -v16, v19, v18
	v_div_fmas_f32 v16, v16, v17, v19
	v_div_fixup_f32 v13, v16, v13, v15
	v_div_scale_f32 v15, s[14:15], v12, v12, v14
	v_rcp_f32_e32 v16, v15
	s_nop 0
	v_fma_f32 v17, -v15, v16, 1.0
	v_fmac_f32_e32 v16, v17, v16
	v_div_scale_f32 v17, vcc, v14, v12, v14
	v_mul_f32_e32 v18, v17, v16
	v_fma_f32 v19, -v15, v18, v17
	v_fmac_f32_e32 v18, v19, v16
	v_fma_f32 v15, -v15, v18, v17
	v_div_fmas_f32 v15, v15, v16, v18
	v_div_fixup_f32 v12, v15, v12, v14
	v_pk_mul_f32 v[10:11], v[12:13], v[10:11]
	v_mul_f32_e32 v12, 0xbfb8aa3b, v4
	v_mul_f32_e32 v13, 0xbfb8aa3b, v5
	v_exp_f32_e32 v12, v12
	v_exp_f32_e32 v13, v13
	s_nop 0
	v_pk_add_f32 v[12:13], v[12:13], 1.0 op_sel_hi:[1,0]
	s_nop 0
	v_div_scale_f32 v14, s[14:15], v13, v13, v5
	v_rcp_f32_e32 v15, v14
	s_nop 0
	v_fma_f32 v16, -v14, v15, 1.0
	v_fmac_f32_e32 v15, v16, v15
	v_div_scale_f32 v16, vcc, v5, v13, v5
	v_mul_f32_e32 v17, v16, v15
	v_fma_f32 v18, -v14, v17, v16
	v_fmac_f32_e32 v17, v18, v15
	v_fma_f32 v14, -v14, v17, v16
	v_div_fmas_f32 v14, v14, v15, v17
	v_div_fixup_f32 v5, v14, v13, v5
	v_div_scale_f32 v13, s[14:15], v12, v12, v4
	v_rcp_f32_e32 v14, v13
	s_nop 0
	v_fma_f32 v15, -v13, v14, 1.0
	v_fmac_f32_e32 v14, v15, v14
	v_div_scale_f32 v15, vcc, v4, v12, v4
	v_mul_f32_e32 v16, v15, v14
	v_fma_f32 v17, -v13, v16, v15
	v_fmac_f32_e32 v16, v17, v14
	v_fma_f32 v13, -v13, v16, v15
	v_div_fmas_f32 v13, v13, v14, v16
	v_div_fixup_f32 v4, v13, v12, v4
	v_pk_mul_f32 v[4:5], v[4:5], v[0:1]
	v_mul_f32_e32 v0, 0xbfb8aa3b, v6
	v_mul_f32_e32 v1, 0xbfb8aa3b, v7
	v_exp_f32_e32 v0, v0
	v_exp_f32_e32 v1, v1
	s_nop 0
	v_pk_add_f32 v[0:1], v[0:1], 1.0 op_sel_hi:[1,0]
	s_nop 0
	v_div_scale_f32 v12, s[14:15], v1, v1, v7
	v_rcp_f32_e32 v13, v12
	s_nop 0
	v_fma_f32 v14, -v12, v13, 1.0
	v_fmac_f32_e32 v13, v14, v13
	v_div_scale_f32 v14, vcc, v7, v1, v7
	v_mul_f32_e32 v15, v14, v13
	v_fma_f32 v16, -v12, v15, v14
	v_fmac_f32_e32 v15, v16, v13
	v_fma_f32 v12, -v12, v15, v14
	v_div_fmas_f32 v12, v12, v13, v15
	v_div_fixup_f32 v1, v12, v1, v7
	v_div_scale_f32 v7, s[14:15], v0, v0, v6
	v_rcp_f32_e32 v12, v7
	s_mov_b64 s[14:15], s[8:9]
	v_fma_f32 v13, -v7, v12, 1.0
	v_fmac_f32_e32 v12, v13, v12
	v_div_scale_f32 v13, vcc, v6, v0, v6
	v_mul_f32_e32 v14, v13, v12
	v_fma_f32 v15, -v7, v14, v13
	v_fmac_f32_e32 v14, v15, v12
	v_fma_f32 v7, -v7, v14, v13
	v_div_fmas_f32 v7, v7, v12, v14
	v_div_fixup_f32 v0, v7, v0, v6
	v_pk_mul_f32 v[6:7], v[0:1], v[2:3]
	v_add_u32_e32 v0, 0xb0, v138
	v_ashrrev_i32_e32 v1, 31, v0
	v_lshlrev_b64 v[0:1], 11, v[0:1]
	v_lshl_add_u64 v[0:1], s[18:19], 0, v[0:1]
	v_lshl_add_u64 v[0:1], v[0:1], 0, s[12:13]
	v_lshl_add_u64 v[0:1], v[0:1], 0, s[16:17]
	v_lshl_add_u64 v[12:13], v[0:1], 0, v[114:115]
	v_cvt_pk_bf16_f32 v0, v8, v9
	v_cvt_pk_bf16_f32 v1, v10, v11
	v_cvt_pk_bf16_f32 v2, v4, v5
	v_cvt_pk_bf16_f32 v3, v6, v7
	s_and_b64 vcc, exec, s[10:11]
	v_mov_b32_e32 v138, v152
	s_mov_b32 s12, s4
	global_store_dwordx4 v[12:13], v[0:3], off sc1
	s_cbranch_vccnz .LBB0_1528

.LBB0_1599:
	v_mov_b32_e32 v146, v140
	v_mov_b32_e32 v144, v141
	s_lshl_b32 s4, s4, 8
	s_add_i32 s4, s4, s35
	s_add_i32 s7, s44, s38
	v_add_u32_e32 v146, s4, v146
	v_lshl_add_u32 v144, v144, 3, s7
	v_ashrrev_i32_e32 v147, 31, v146
	v_readlane_b32 s14, v253, 56
	v_ashrrev_i32_e32 v145, 31, v144
	v_lshlrev_b64 v[148:149], 12, v[146:147]
	v_readlane_b32 s15, v253, 57
	v_lshlrev_b64 v[150:151], 1, v[144:145]
	v_cvt_pk_bf16_f32 v122, v122, v123
	v_lshl_add_u64 v[148:149], s[14:15], 0, v[148:149]
	v_lshl_add_u64 v[152:153], v[148:149], 0, v[150:151]
	v_cvt_pk_bf16_f32 v123, v124, v125
	v_cvt_pk_bf16_f32 v124, v126, v127
	v_cvt_pk_bf16_f32 v125, v128, v129
	global_store_dwordx4 v[152:153], v[122:125], off sc1
	v_cvt_pk_bf16_f32 v118, v118, v119
	v_cvt_pk_bf16_f32 v119, v120, v121
	v_add_u32_e32 v122, 16, v146
	v_cvt_pk_bf16_f32 v120, v114, v115
	v_add_u32_e32 v114, 32, v146
	v_cvt_pk_bf16_f32 v110, v110, v111
	v_cvt_pk_bf16_f32 v111, v112, v113
	v_cvt_pk_bf16_f32 v112, v106, v107
	v_add_u32_e32 v106, 48, v146
	v_cvt_pk_bf16_f32 v102, v102, v103
	v_cvt_pk_bf16_f32 v103, v104, v105
	v_cvt_pk_bf16_f32 v104, v98, v99
	v_add_u32_e32 v98, 0x80, v146
	v_cvt_pk_bf16_f32 v92, v92, v93
	v_cvt_pk_bf16_f32 v93, v94, v95
	v_cvt_pk_bf16_f32 v94, v88, v89
	v_add_u32_e32 v88, 0x90, v146
	v_cvt_pk_bf16_f32 v84, v84, v85
	v_cvt_pk_bf16_f32 v85, v86, v87
	v_cvt_pk_bf16_f32 v86, v80, v81
	v_add_u32_e32 v80, 0xa0, v146
	v_cvt_pk_bf16_f32 v76, v76, v77
	v_cvt_pk_bf16_f32 v77, v78, v79
	v_cvt_pk_bf16_f32 v78, v72, v73
	v_add_u32_e32 v72, 0xb0, v146
	v_ashrrev_i32_e32 v123, 31, v122
	v_ashrrev_i32_e32 v115, 31, v114
	v_ashrrev_i32_e32 v107, 31, v106
	v_ashrrev_i32_e32 v99, 31, v98
	v_ashrrev_i32_e32 v89, 31, v88
	v_ashrrev_i32_e32 v81, 31, v80
	v_ashrrev_i32_e32 v73, 31, v72
	v_cvt_pk_bf16_f32 v68, v68, v69
	v_cvt_pk_bf16_f32 v69, v70, v71
	v_cvt_pk_bf16_f32 v70, v64, v65
	v_add_u32_e32 v64, 0x80, v144
	v_lshlrev_b64 v[122:123], 12, v[122:123]
	v_lshlrev_b64 v[114:115], 12, v[114:115]
	v_lshlrev_b64 v[106:107], 12, v[106:107]
	v_lshlrev_b64 v[98:99], 12, v[98:99]
	v_lshlrev_b64 v[88:89], 12, v[88:89]
	v_lshlrev_b64 v[80:81], 12, v[80:81]
	v_lshlrev_b64 v[72:73], 12, v[72:73]
	v_ashrrev_i32_e32 v65, 31, v64
	v_lshl_add_u64 v[122:123], s[14:15], 0, v[122:123]
	v_lshl_add_u64 v[114:115], s[14:15], 0, v[114:115]
	v_lshl_add_u64 v[106:107], s[14:15], 0, v[106:107]
	v_lshl_add_u64 v[98:99], s[14:15], 0, v[98:99]
	v_lshl_add_u64 v[88:89], s[14:15], 0, v[88:89]
	v_lshl_add_u64 v[80:81], s[14:15], 0, v[80:81]
	v_lshl_add_u64 v[72:73], s[14:15], 0, v[72:73]
	v_lshlrev_b64 v[64:65], 1, v[64:65]
	v_lshl_add_u64 v[124:125], v[122:123], 0, v[150:151]
	v_cvt_pk_bf16_f32 v121, v116, v117
	v_lshl_add_u64 v[116:117], v[114:115], 0, v[150:151]
	v_cvt_pk_bf16_f32 v113, v108, v109
	v_lshl_add_u64 v[108:109], v[106:107], 0, v[150:151]
	v_cvt_pk_bf16_f32 v105, v100, v101
	v_lshl_add_u64 v[100:101], v[98:99], 0, v[150:151]
	v_cvt_pk_bf16_f32 v95, v90, v91
	v_lshl_add_u64 v[90:91], v[88:89], 0, v[150:151]
	v_cvt_pk_bf16_f32 v87, v82, v83
	v_lshl_add_u64 v[82:83], v[80:81], 0, v[150:151]
	v_cvt_pk_bf16_f32 v79, v74, v75
	v_lshl_add_u64 v[74:75], v[72:73], 0, v[150:151]
	v_cvt_pk_bf16_f32 v71, v66, v67
	v_lshl_add_u64 v[66:67], v[148:149], 0, v[64:65]
	v_cvt_pk_bf16_f32 v60, v60, v61
	v_cvt_pk_bf16_f32 v61, v62, v63
	v_cvt_pk_bf16_f32 v62, v56, v57
	v_cvt_pk_bf16_f32 v63, v58, v59
	v_lshl_add_u64 v[56:57], v[122:123], 0, v[64:65]
	v_cvt_pk_bf16_f32 v52, v52, v53
	v_cvt_pk_bf16_f32 v53, v54, v55
	v_cvt_pk_bf16_f32 v54, v48, v49
	v_cvt_pk_bf16_f32 v55, v50, v51
	v_lshl_add_u64 v[48:49], v[114:115], 0, v[64:65]
	v_cvt_pk_bf16_f32 v44, v44, v45
	v_cvt_pk_bf16_f32 v45, v46, v47
	v_cvt_pk_bf16_f32 v46, v40, v41
	v_cvt_pk_bf16_f32 v47, v42, v43
	v_lshl_add_u64 v[40:41], v[106:107], 0, v[64:65]
	v_cvt_pk_bf16_f32 v36, v36, v37
	v_cvt_pk_bf16_f32 v37, v38, v39
	v_cvt_pk_bf16_f32 v38, v32, v33
	v_cvt_pk_bf16_f32 v39, v34, v35
	v_lshl_add_u64 v[32:33], v[98:99], 0, v[64:65]
	v_cvt_pk_bf16_f32 v28, v28, v29
	v_cvt_pk_bf16_f32 v29, v30, v31
	v_cvt_pk_bf16_f32 v30, v24, v25
	v_cvt_pk_bf16_f32 v31, v26, v27
	v_lshl_add_u64 v[24:25], v[88:89], 0, v[64:65]
	v_cvt_pk_bf16_f32 v20, v20, v21
	v_cvt_pk_bf16_f32 v21, v22, v23
	v_cvt_pk_bf16_f32 v22, v16, v17
	v_cvt_pk_bf16_f32 v23, v18, v19
	v_lshl_add_u64 v[16:17], v[80:81], 0, v[64:65]
	v_cvt_pk_bf16_f32 v12, v12, v13
	v_cvt_pk_bf16_f32 v13, v14, v15
	v_cvt_pk_bf16_f32 v14, v8, v9
	v_cvt_pk_bf16_f32 v15, v10, v11
	v_lshl_add_u64 v[8:9], v[72:73], 0, v[64:65]
	v_cvt_pk_bf16_f32 v4, v4, v5
	v_cvt_pk_bf16_f32 v5, v6, v7
	v_cvt_pk_bf16_f32 v6, v0, v1
	v_cvt_pk_bf16_f32 v7, v2, v3
	s_and_b64 vcc, exec, s[10:11]
	s_mov_b32 s44, s43
	s_mov_b32 s4, s6
	s_mov_b64 s[18:19], s[12:13]
	s_mov_b64 s[14:15], s[8:9]
	global_store_dwordx4 v[124:125], v[118:121], off sc1
	global_store_dwordx4 v[116:117], v[110:113], off sc1
	global_store_dwordx4 v[108:109], v[102:105], off sc1
	global_store_dwordx4 v[100:101], v[92:95], off sc1
	global_store_dwordx4 v[90:91], v[84:87], off sc1
	global_store_dwordx4 v[82:83], v[76:79], off sc1
	global_store_dwordx4 v[74:75], v[68:71], off sc1
	global_store_dwordx4 v[66:67], v[60:63], off sc1
	global_store_dwordx4 v[56:57], v[52:55], off sc1
	global_store_dwordx4 v[48:49], v[44:47], off sc1
	global_store_dwordx4 v[40:41], v[36:39], off sc1
	global_store_dwordx4 v[32:33], v[28:31], off sc1
	global_store_dwordx4 v[24:25], v[20:23], off sc1
	global_store_dwordx4 v[16:17], v[12:15], off sc1
	global_store_dwordx4 v[8:9], v[4:7], off sc1
	s_cbranch_vccnz .LBB0_1605
